# P2 rewrite + conv counted waits + write-through sc1 stores in P1/P3/P9 GEMM epilogues
# baseline (speedup 1.0000x reference)
; #define LAS __attribute__((address_space(3)))
; __device__ __forceinline__ unsigned cvt_pk_bf16(float lo, float hi) { unsigned r; asm volatile("v_cvt_pk_bf16_f32 %0, %1, %2" : "=v"(r) : "v"(lo), "v"(hi)); return r; }
;     __device__ void operator()(int r, int n, float v) const { if (r < NMETA) proj[(size_t)(M + r) * DINP + n] = f2bf(v); }
;     __device__ __forceinline__ void operator()(const f32x4 (&acc)[2][2][4][2], const Unit& u, int wr, int wc, int fr, int fq, const LAS float* bl) const {
;         const int row0 = u.pm * BM + wr * 64 + fr, col0 = u.pn * BM + wc * 32 + 8 * fq;
; #pragma unroll
;         for (int ai = 0; ai < 2; ++ai)
; #pragma unroll
;             for (int m = 0; m < 4; ++m) { bf16* rowp = O + (size_t)(row0 + ai * HALF + m * 16) * ldc + col0;
; #pragma unroll
;                 for (int bj = 0; bj < 2; ++bj) { const f32x4 v0 = acc[ai][bj][m][0], v1 = acc[ai][bj][m][1];
;                     u32x4 w; w.x = cvt_pk_bf16(v0[0], v0[1]); w.y = cvt_pk_bf16(v0[2], v0[3]); w.z = cvt_pk_bf16(v1[0], v1[1]); w.w = cvt_pk_bf16(v1[2], v1[3]);
;                     *(u32x4*)(rowp + bj * HALF) = w; } }
;     }
.LBB0_193:
	v_lshl_add_u32 v132, s84, 8, v214
	v_lshl_or_b32 v130, s60, 8, v215
	v_ashrrev_i32_e32 v133, 31, v132
	v_ashrrev_i32_e32 v131, 31, v130
	v_lshlrev_b64 v[134:135], 13, v[132:133]
	v_lshl_add_u64 v[134:135], s[36:37], 0, v[134:135]
	v_lshlrev_b64 v[136:137], 1, v[130:131]
	v_lshl_add_u64 v[130:131], v[134:135], 0, v[136:137]
	v_cvt_pk_bf16_f32 v126, v126, v127
	v_cvt_pk_bf16_f32 v127, v128, v129
	v_cvt_pk_bf16_f32 v128, v122, v123
	v_cvt_pk_bf16_f32 v129, v124, v125
	global_store_dwordx4 v[130:131], v[126:129], off sc1
	v_cvt_pk_bf16_f32 v118, v118, v119
	v_cvt_pk_bf16_f32 v119, v120, v121
	v_cvt_pk_bf16_f32 v120, v114, v115
	v_or_b32_e32 v114, 16, v132
	v_ashrrev_i32_e32 v115, 31, v114
	v_lshlrev_b64 v[114:115], 13, v[114:115]
	v_lshl_add_u64 v[114:115], s[36:37], 0, v[114:115]
	v_lshl_add_u64 v[114:115], v[114:115], 0, v[136:137]
	v_cvt_pk_bf16_f32 v121, v116, v117
	global_store_dwordx4 v[130:131], v[118:121], off offset:256 sc1
	v_cvt_pk_bf16_f32 v110, v110, v111
	v_cvt_pk_bf16_f32 v111, v112, v113
	v_cvt_pk_bf16_f32 v112, v106, v107
	v_cvt_pk_bf16_f32 v113, v108, v109
	global_store_dwordx4 v[114:115], v[110:113], off sc1
	v_cvt_pk_bf16_f32 v102, v102, v103
	v_cvt_pk_bf16_f32 v103, v104, v105
	v_cvt_pk_bf16_f32 v104, v98, v99
	v_or_b32_e32 v98, 32, v132
	v_ashrrev_i32_e32 v99, 31, v98
	v_lshlrev_b64 v[98:99], 13, v[98:99]
	v_lshl_add_u64 v[98:99], s[36:37], 0, v[98:99]
	v_lshl_add_u64 v[98:99], v[98:99], 0, v[136:137]
	v_cvt_pk_bf16_f32 v105, v100, v101
	global_store_dwordx4 v[114:115], v[102:105], off offset:256 sc1
	v_cvt_pk_bf16_f32 v94, v94, v95
	v_cvt_pk_bf16_f32 v95, v96, v97
	v_cvt_pk_bf16_f32 v96, v90, v91
	v_cvt_pk_bf16_f32 v97, v92, v93
	global_store_dwordx4 v[98:99], v[94:97], off sc1
	v_cvt_pk_bf16_f32 v86, v86, v87
	v_cvt_pk_bf16_f32 v87, v88, v89
	v_cvt_pk_bf16_f32 v88, v82, v83
	v_or_b32_e32 v82, 48, v132
	v_ashrrev_i32_e32 v83, 31, v82
	v_lshlrev_b64 v[82:83], 13, v[82:83]
	v_lshl_add_u64 v[82:83], s[36:37], 0, v[82:83]
	v_lshl_add_u64 v[82:83], v[82:83], 0, v[136:137]
	v_cvt_pk_bf16_f32 v89, v84, v85
	global_store_dwordx4 v[98:99], v[86:89], off offset:256 sc1
	v_cvt_pk_bf16_f32 v78, v78, v79
	v_cvt_pk_bf16_f32 v79, v80, v81
	v_cvt_pk_bf16_f32 v80, v74, v75
	v_cvt_pk_bf16_f32 v81, v76, v77
	global_store_dwordx4 v[82:83], v[78:81], off sc1
	v_cvt_pk_bf16_f32 v70, v70, v71
	v_cvt_pk_bf16_f32 v71, v72, v73
	v_cvt_pk_bf16_f32 v72, v66, v67
	v_cvt_pk_bf16_f32 v73, v68, v69
	global_store_dwordx4 v[82:83], v[70:73], off offset:256 sc1
	v_cvt_pk_bf16_f32 v62, v62, v63
	v_cvt_pk_bf16_f32 v63, v64, v65
	v_cvt_pk_bf16_f32 v64, v58, v59
	v_add_co_u32_e32 v58, vcc, s79, v130
	v_lshl_add_u64 v[66:67], v[130:131], 0, s[50:51]
	s_nop 0
	v_addc_co_u32_e32 v59, vcc, 0, v131, vcc
	v_cvt_pk_bf16_f32 v65, v60, v61
	global_store_dwordx4 v[58:59], v[62:65], off sc1
	v_cvt_pk_bf16_f32 v54, v54, v55
	v_cvt_pk_bf16_f32 v55, v56, v57
	v_cvt_pk_bf16_f32 v56, v50, v51
	v_cvt_pk_bf16_f32 v57, v52, v53
	global_store_dwordx4 v[66:67], v[54:57], off offset:256 sc1
	v_cvt_pk_bf16_f32 v46, v46, v47
	v_cvt_pk_bf16_f32 v47, v48, v49
	v_cvt_pk_bf16_f32 v48, v42, v43
	v_add_co_u32_e32 v42, vcc, s80, v130
	v_lshl_add_u64 v[50:51], v[130:131], 0, s[52:53]
	s_nop 0
	v_addc_co_u32_e32 v43, vcc, 0, v131, vcc
	v_cvt_pk_bf16_f32 v49, v44, v45
	global_store_dwordx4 v[42:43], v[46:49], off sc1
	v_cvt_pk_bf16_f32 v38, v38, v39
	v_cvt_pk_bf16_f32 v39, v40, v41
	v_cvt_pk_bf16_f32 v40, v22, v23
	v_cvt_pk_bf16_f32 v41, v24, v25
	global_store_dwordx4 v[50:51], v[38:41], off offset:256 sc1
	v_cvt_pk_bf16_f32 v22, v30, v31
	v_cvt_pk_bf16_f32 v23, v32, v33
	v_cvt_pk_bf16_f32 v24, v18, v19
	v_add_co_u32_e32 v18, vcc, s81, v130
	s_nop 0
	v_lshl_add_u64 v[38:39], v[130:131], 0, s[54:55]
	v_addc_co_u32_e32 v19, vcc, 0, v131, vcc
	v_cvt_pk_bf16_f32 v25, v20, v21
	global_store_dwordx4 v[18:19], v[22:25], off sc1
	v_cvt_pk_bf16_f32 v18, v34, v35
	v_cvt_pk_bf16_f32 v19, v36, v37
	v_cvt_pk_bf16_f32 v20, v26, v27
	v_cvt_pk_bf16_f32 v21, v28, v29
	global_store_dwordx4 v[38:39], v[18:21], off offset:256 sc1
	v_cvt_pk_bf16_f32 v6, v6, v7
	v_cvt_pk_bf16_f32 v7, v8, v9
	v_cvt_pk_bf16_f32 v8, v2, v3
	v_add_co_u32_e32 v2, vcc, s82, v130
	s_nop 0
	v_lshl_add_u64 v[18:19], v[130:131], 0, s[56:57]
	v_addc_co_u32_e32 v3, vcc, 0, v131, vcc
	s_andn2_b64 vcc, exec, s[4:5]
	s_mov_b64 s[4:5], -1
	v_cvt_pk_bf16_f32 v9, v4, v5
	global_store_dwordx4 v[2:3], v[6:9], off sc1
	v_cvt_pk_bf16_f32 v2, v14, v15
	v_cvt_pk_bf16_f32 v3, v16, v17
	v_cvt_pk_bf16_f32 v4, v10, v11
	v_cvt_pk_bf16_f32 v5, v12, v13
	global_store_dwordx4 v[18:19], v[2:5], off offset:256 sc1
	s_cbranch_vccnz .LBB0_172
	s_andn2_b64 vcc, exec, s[10:11]
	s_cbranch_vccnz .LBB0_171
	s_barrier
	s_branch .LBB0_171

; #define LAS __attribute__((address_space(3)))
; __device__ __forceinline__ unsigned cvt_pk_bf16(float lo, float hi) { unsigned r; asm volatile("v_cvt_pk_bf16_f32 %0, %1, %2" : "=v"(r) : "v"(lo), "v"(hi)); return r; }
;     __device__ void operator()(int r, int n, float v) const { if (r < NMETA) proj[(size_t)(M + r) * DINP + n] = f2bf(v); }
;     __device__ __forceinline__ void operator()(const f32x4 (&acc)[2][2][4][2], const Unit& u, int wr, int wc, int fr, int fq, const LAS float* bl) const {
;         const int row0 = u.pm * BM + wr * 64 + fr;
; #pragma unroll
;         for (int bj = 0; bj < 2; ++bj) {
;             const int k64 = 4 * u.pn + 2 * bj + (wc >> 1), head = k64 / 3, type = k64 % 3, blk = wc & 1;
;             if (type < 2) {
;                 const int dim = 64 * type + 32 * blk + 8 * fq;
; #pragma unroll
;                 for (int ai = 0; ai < 2; ++ai)
; #pragma unroll
;                     for (int m = 0; m < 4; ++m) { const int r = row0 + ai * HALF + m * 16; const f32x4 v0 = acc[ai][bj][m][0], v1 = acc[ai][bj][m][1];
;                         u32x4 w; w.x = cvt_pk_bf16(v0[0], v0[1]); w.y = cvt_pk_bf16(v0[2], v0[3]); w.z = cvt_pk_bf16(v1[0], v1[1]); w.w = cvt_pk_bf16(v1[2], v1[3]);
;                         *(u32x4*)(Q + ((size_t)r * NH + head) * DQK + dim) = w; }
;             } else {
;                 const int i0 = 16 * blk + 4 * fq;
; #pragma unroll
;                 for (int ai = 0; ai < 2; ++ai)
; #pragma unroll
;                     for (int m = 0; m < 4; ++m) { const int r = row0 + ai * HALF + m * 16, pos = (r % S) + NMETA;
;                         const f32x4 cs = *(const f32x4*)(cosT + pos * 32 + i0), sn = *(const f32x4*)(sinT + pos * 32 + i0);
;                         const f32x4 x1 = acc[ai][bj][m][0], x2 = acc[ai][bj][m][1];
;                         const f32x4 o1 = x1 * cs - x2 * sn, o2 = x1 * sn + x2 * cs;
;                         bf16* dst = Q + ((size_t)r * NH + head) * DQK + 128 + i0;
;                         u32x2 w1; w1.x = cvt_pk_bf16(o1[0], o1[1]); w1.y = cvt_pk_bf16(o1[2], o1[3]); *(u32x2*)(dst) = w1;
;                         u32x2 w2; w2.x = cvt_pk_bf16(o2[0], o2[1]); w2.y = cvt_pk_bf16(o2[2], o2[3]); *(u32x2*)(dst + 32) = w2; }
.LBB0_480:
	s_lshl_b32 s6, s74, 2
	v_lshl_add_u32 v136, s19, 8, v221
	s_or_b32 s19, s6, s16
	s_mul_hi_i32 s6, s19, 0x55555556
	s_lshr_b32 s7, s6, 31
	s_add_i32 s6, s6, s7
	s_mul_i32 s7, s6, 3
	s_sub_i32 s28, s19, s7
	v_ashrrev_i32_e32 v137, 31, v136
	v_or_b32_e32 v134, 16, v136
	v_or_b32_e32 v132, 32, v136
	v_or_b32_e32 v130, 48, v136
	v_add_u32_e32 v144, 0x80, v136
	v_add_u32_e32 v142, 0x90, v136
	v_add_u32_e32 v140, 0xa0, v136
	s_mov_b64 s[8:9], -1
	s_cmp_gt_i32 s28, 1
	v_lshrrev_b32_e32 v146, 20, v137
	v_ashrrev_i32_e32 v135, 31, v134
	v_ashrrev_i32_e32 v133, 31, v132
	v_ashrrev_i32_e32 v131, 31, v130
	v_ashrrev_i32_e32 v145, 31, v144
	v_ashrrev_i32_e32 v143, 31, v142
	v_ashrrev_i32_e32 v141, 31, v140
	v_add_u32_e32 v138, 0xb0, v136
	s_cbranch_scc0 .LBB0_482
	v_add_u32_e32 v139, v136, v146
	v_and_b32_e32 v139, 0x7fff000, v139
	v_sub_u32_e32 v139, v136, v139
	v_lshlrev_b32_e32 v148, 5, v139
	v_ashrrev_i32_e32 v149, 31, v148
	v_lshlrev_b64 v[152:153], 2, v[148:149]
	v_lshl_add_u64 v[148:149], v[204:205], 0, v[152:153]
	global_load_dwordx4 v[148:151], v[148:149], off offset:2048
	v_lshl_add_u64 v[152:153], v[202:203], 0, v[152:153]
	global_load_dwordx4 v[152:155], v[152:153], off offset:2048
	v_add_u32_e32 v139, v134, v146
	s_ashr_i32 s7, s6, 31
	v_and_b32_e32 v139, 0x7fff000, v139
	v_lshl_add_u64 v[156:157], v[136:137], 3, s[6:7]
	v_sub_u32_e32 v139, v134, v139
	v_mad_u64_u32 v[158:159], s[8:9], v156, s25, v[206:207]
	v_lshlrev_b32_e32 v156, 5, v139
	v_mad_i32_i24 v159, v157, s25, v159
	v_ashrrev_i32_e32 v157, 31, v156
	v_lshlrev_b64 v[156:157], 2, v[156:157]
	v_lshl_add_u64 v[160:161], v[204:205], 0, v[156:157]
	v_add_u32_e32 v139, v132, v146
	v_and_b32_e32 v139, 0x7fff000, v139
	v_sub_u32_e32 v139, v132, v139
	s_waitcnt vmcnt(0) lgkmcnt(0)
	v_pk_mul_f32 v[164:165], v[122:123], v[148:149]
	v_pk_mul_f32 v[148:149], v[126:127], v[148:149]
	v_pk_mul_f32 v[162:163], v[124:125], v[150:151]
	v_pk_mul_f32 v[150:151], v[128:129], v[150:151]
	v_pk_fma_f32 v[148:149], v[122:123], v[152:153], v[148:149]
	v_pk_fma_f32 v[162:163], v[128:129], v[154:155], v[162:163] neg_lo:[0,0,1] neg_hi:[0,0,1]
	v_pk_fma_f32 v[164:165], v[126:127], v[152:153], v[164:165] neg_lo:[0,0,1] neg_hi:[0,0,1]
	v_pk_fma_f32 v[150:151], v[124:125], v[154:155], v[150:151]
	v_cvt_pk_bf16_f32 v152, v164, v165
	v_cvt_pk_bf16_f32 v153, v162, v163
	global_store_dwordx2 v[158:159], v[152:153], off offset:256 sc1
	v_cvt_pk_bf16_f32 v148, v148, v149
	v_cvt_pk_bf16_f32 v149, v150, v151
	global_store_dwordx2 v[158:159], v[148:149], off offset:320 sc1
	global_load_dwordx4 v[148:151], v[160:161], off offset:2048
	v_lshl_add_u64 v[152:153], v[202:203], 0, v[156:157]
	global_load_dwordx4 v[152:155], v[152:153], off offset:2048
	v_lshl_add_u64 v[156:157], v[134:135], 3, s[6:7]
	v_mad_u64_u32 v[158:159], s[8:9], v156, s25, v[206:207]
	v_lshlrev_b32_e32 v156, 5, v139
	v_mad_i32_i24 v159, v157, s25, v159
	v_ashrrev_i32_e32 v157, 31, v156
	v_lshlrev_b64 v[156:157], 2, v[156:157]
	v_lshl_add_u64 v[160:161], v[204:205], 0, v[156:157]
	v_add_u32_e32 v139, v130, v146
	v_and_b32_e32 v139, 0x7fff000, v139
	v_sub_u32_e32 v139, v130, v139
	s_waitcnt vmcnt(1)
	v_pk_mul_f32 v[164:165], v[114:115], v[148:149]
	v_pk_mul_f32 v[148:149], v[118:119], v[148:149]
	v_pk_mul_f32 v[162:163], v[116:117], v[150:151]
	v_pk_mul_f32 v[150:151], v[120:121], v[150:151]
	s_waitcnt vmcnt(0)
	v_pk_fma_f32 v[148:149], v[114:115], v[152:153], v[148:149]
	v_pk_fma_f32 v[162:163], v[120:121], v[154:155], v[162:163] neg_lo:[0,0,1] neg_hi:[0,0,1]
	v_pk_fma_f32 v[164:165], v[118:119], v[152:153], v[164:165] neg_lo:[0,0,1] neg_hi:[0,0,1]
	v_pk_fma_f32 v[150:151], v[116:117], v[154:155], v[150:151]
	v_cvt_pk_bf16_f32 v152, v164, v165
	v_cvt_pk_bf16_f32 v153, v162, v163
	global_store_dwordx2 v[158:159], v[152:153], off offset:256 sc1
	v_cvt_pk_bf16_f32 v148, v148, v149
	v_cvt_pk_bf16_f32 v149, v150, v151
	global_store_dwordx2 v[158:159], v[148:149], off offset:320 sc1
	global_load_dwordx4 v[148:151], v[160:161], off offset:2048
	v_lshl_add_u64 v[152:153], v[202:203], 0, v[156:157]
	global_load_dwordx4 v[152:155], v[152:153], off offset:2048
	v_lshl_add_u64 v[156:157], v[132:133], 3, s[6:7]
	v_mad_u64_u32 v[158:159], s[8:9], v156, s25, v[206:207]
	v_lshlrev_b32_e32 v156, 5, v139
	v_mad_i32_i24 v159, v157, s25, v159
	v_ashrrev_i32_e32 v157, 31, v156
	v_lshlrev_b64 v[156:157], 2, v[156:157]
	v_lshl_add_u64 v[160:161], v[204:205], 0, v[156:157]
	v_lshrrev_b32_e32 v139, 20, v145
	v_add_u32_e32 v139, v144, v139
	v_and_b32_e32 v139, 0x7fff000, v139
	v_sub_u32_e32 v139, v144, v139
	s_waitcnt vmcnt(1)
	v_pk_mul_f32 v[164:165], v[106:107], v[148:149]
	v_pk_mul_f32 v[148:149], v[110:111], v[148:149]
	v_pk_mul_f32 v[162:163], v[108:109], v[150:151]
	v_pk_mul_f32 v[150:151], v[112:113], v[150:151]
	s_waitcnt vmcnt(0)
	v_pk_fma_f32 v[148:149], v[106:107], v[152:153], v[148:149]
	v_pk_fma_f32 v[162:163], v[112:113], v[154:155], v[162:163] neg_lo:[0,0,1] neg_hi:[0,0,1]
	v_pk_fma_f32 v[164:165], v[110:111], v[152:153], v[164:165] neg_lo:[0,0,1] neg_hi:[0,0,1]
	v_pk_fma_f32 v[150:151], v[108:109], v[154:155], v[150:151]
	v_cvt_pk_bf16_f32 v152, v164, v165
	v_cvt_pk_bf16_f32 v153, v162, v163
	global_store_dwordx2 v[158:159], v[152:153], off offset:256 sc1
	v_cvt_pk_bf16_f32 v148, v148, v149
	v_cvt_pk_bf16_f32 v149, v150, v151
	global_store_dwordx2 v[158:159], v[148:149], off offset:320 sc1
	global_load_dwordx4 v[148:151], v[160:161], off offset:2048
	v_lshl_add_u64 v[152:153], v[202:203], 0, v[156:157]
	global_load_dwordx4 v[152:155], v[152:153], off offset:2048
	v_lshl_add_u64 v[156:157], v[130:131], 3, s[6:7]
	v_mad_u64_u32 v[158:159], s[8:9], v156, s25, v[206:207]
	v_lshlrev_b32_e32 v156, 5, v139
	v_mad_i32_i24 v159, v157, s25, v159
	v_ashrrev_i32_e32 v157, 31, v156
	v_lshlrev_b64 v[156:157], 2, v[156:157]
	v_lshl_add_u64 v[160:161], v[204:205], 0, v[156:157]
	v_lshrrev_b32_e32 v139, 20, v143
	v_add_u32_e32 v139, v142, v139
	v_and_b32_e32 v139, 0x7fff000, v139
	v_sub_u32_e32 v139, v142, v139
	s_waitcnt vmcnt(1)
; __device__ __forceinline__ unsigned cvt_pk_bf16(float lo, float hi) { unsigned r; asm volatile("v_cvt_pk_bf16_f32 %0, %1, %2" : "=v"(r) : "v"(lo), "v"(hi)); return r; }
;     __device__ __forceinline__ void operator()(const f32x4 (&acc)[2][2][4][2], const Unit& u, int wr, int wc, int fr, int fq, const LAS float* bl) const {
;     ...
;                     for (int m = 0; m < 4; ++m) { const int r = row0 + ai * HALF + m * 16; const f32x4 v0 = acc[ai][bj][m][0], v1 = acc[ai][bj][m][1];
;                         u32x4 w; w.x = cvt_pk_bf16(v0[0], v0[1]); w.y = cvt_pk_bf16(v0[2], v0[3]); w.z = cvt_pk_bf16(v1[0], v1[1]); w.w = cvt_pk_bf16(v1[2], v1[3]);
;                         *(u32x4*)(Q + ((size_t)r * NH + head) * DQK + dim) = w; }
;             } else {
;                 const int i0 = 16 * blk + 4 * fq;
; #pragma unroll
;                 for (int ai = 0; ai < 2; ++ai)
; #pragma unroll
;                     for (int m = 0; m < 4; ++m) { const int r = row0 + ai * HALF + m * 16, pos = (r % S) + NMETA;
;                         const f32x4 cs = *(const f32x4*)(cosT + pos * 32 + i0), sn = *(const f32x4*)(sinT + pos * 32 + i0);
;                         const f32x4 x1 = acc[ai][bj][m][0], x2 = acc[ai][bj][m][1];
;                         const f32x4 o1 = x1 * cs - x2 * sn, o2 = x1 * sn + x2 * cs;
;                         bf16* dst = Q + ((size_t)r * NH + head) * DQK + 128 + i0;
;                         u32x2 w1; w1.x = cvt_pk_bf16(o1[0], o1[1]); w1.y = cvt_pk_bf16(o1[2], o1[3]); *(u32x2*)(dst) = w1;
;                         u32x2 w2; w2.x = cvt_pk_bf16(o2[0], o2[1]); w2.y = cvt_pk_bf16(o2[2], o2[3]); *(u32x2*)(dst + 32) = w2; }
	v_pk_mul_f32 v[164:165], v[98:99], v[148:149]
	v_pk_mul_f32 v[148:149], v[102:103], v[148:149]
	v_pk_mul_f32 v[162:163], v[100:101], v[150:151]
	v_pk_mul_f32 v[150:151], v[104:105], v[150:151]
	s_waitcnt vmcnt(0)
	v_pk_fma_f32 v[148:149], v[98:99], v[152:153], v[148:149]
	v_pk_fma_f32 v[162:163], v[104:105], v[154:155], v[162:163] neg_lo:[0,0,1] neg_hi:[0,0,1]
	v_pk_fma_f32 v[164:165], v[102:103], v[152:153], v[164:165] neg_lo:[0,0,1] neg_hi:[0,0,1]
	v_pk_fma_f32 v[150:151], v[100:101], v[154:155], v[150:151]
	v_cvt_pk_bf16_f32 v152, v164, v165
	v_cvt_pk_bf16_f32 v153, v162, v163
	global_store_dwordx2 v[158:159], v[152:153], off offset:256 sc1
	v_cvt_pk_bf16_f32 v148, v148, v149
	v_cvt_pk_bf16_f32 v149, v150, v151
	global_store_dwordx2 v[158:159], v[148:149], off offset:320 sc1
	global_load_dwordx4 v[148:151], v[160:161], off offset:2048
	v_lshl_add_u64 v[152:153], v[202:203], 0, v[156:157]
	global_load_dwordx4 v[152:155], v[152:153], off offset:2048
	v_lshl_add_u64 v[156:157], v[144:145], 3, s[6:7]
	v_mad_u64_u32 v[158:159], s[8:9], v156, s25, v[206:207]
	v_lshlrev_b32_e32 v156, 5, v139
	v_mad_i32_i24 v159, v157, s25, v159
	v_ashrrev_i32_e32 v157, 31, v156
	v_lshlrev_b64 v[156:157], 2, v[156:157]
	v_lshl_add_u64 v[160:161], v[204:205], 0, v[156:157]
	v_lshrrev_b32_e32 v139, 20, v141
	v_add_u32_e32 v139, v140, v139
	v_and_b32_e32 v139, 0x7fff000, v139
	v_sub_u32_e32 v139, v140, v139
	s_waitcnt vmcnt(1)
	v_pk_mul_f32 v[164:165], v[90:91], v[148:149]
	v_pk_mul_f32 v[148:149], v[94:95], v[148:149]
	v_pk_mul_f32 v[162:163], v[92:93], v[150:151]
	v_pk_mul_f32 v[150:151], v[96:97], v[150:151]
	s_waitcnt vmcnt(0)
	v_pk_fma_f32 v[148:149], v[90:91], v[152:153], v[148:149]
	v_pk_fma_f32 v[162:163], v[96:97], v[154:155], v[162:163] neg_lo:[0,0,1] neg_hi:[0,0,1]
	v_pk_fma_f32 v[164:165], v[94:95], v[152:153], v[164:165] neg_lo:[0,0,1] neg_hi:[0,0,1]
	v_pk_fma_f32 v[150:151], v[92:93], v[154:155], v[150:151]
	v_cvt_pk_bf16_f32 v152, v164, v165
	v_cvt_pk_bf16_f32 v153, v162, v163
	global_store_dwordx2 v[158:159], v[152:153], off offset:256 sc1
	v_cvt_pk_bf16_f32 v148, v148, v149
	v_cvt_pk_bf16_f32 v149, v150, v151
	global_store_dwordx2 v[158:159], v[148:149], off offset:320 sc1
	global_load_dwordx4 v[148:151], v[160:161], off offset:2048
	v_lshl_add_u64 v[152:153], v[202:203], 0, v[156:157]
	global_load_dwordx4 v[152:155], v[152:153], off offset:2048
	v_lshl_add_u64 v[156:157], v[142:143], 3, s[6:7]
	v_mad_u64_u32 v[158:159], s[8:9], v156, s25, v[206:207]
	v_lshlrev_b32_e32 v156, 5, v139
	v_mad_i32_i24 v159, v157, s25, v159
	v_ashrrev_i32_e32 v157, 31, v156
	v_lshlrev_b64 v[156:157], 2, v[156:157]
	v_lshl_add_u64 v[160:161], v[204:205], 0, v[156:157]
	v_ashrrev_i32_e32 v139, 31, v138
	v_lshrrev_b32_e32 v147, 20, v139
	v_add_u32_e32 v147, v138, v147
	v_and_b32_e32 v147, 0x7fff000, v147
	v_sub_u32_e32 v147, v138, v147
	s_waitcnt vmcnt(1)
	v_pk_mul_f32 v[164:165], v[82:83], v[148:149]
	v_pk_mul_f32 v[148:149], v[86:87], v[148:149]
	v_pk_mul_f32 v[162:163], v[84:85], v[150:151]
	v_pk_mul_f32 v[150:151], v[88:89], v[150:151]
	s_waitcnt vmcnt(0)
	v_pk_fma_f32 v[148:149], v[82:83], v[152:153], v[148:149]
	v_pk_fma_f32 v[162:163], v[88:89], v[154:155], v[162:163] neg_lo:[0,0,1] neg_hi:[0,0,1]
	v_pk_fma_f32 v[164:165], v[86:87], v[152:153], v[164:165] neg_lo:[0,0,1] neg_hi:[0,0,1]
	v_pk_fma_f32 v[150:151], v[84:85], v[154:155], v[150:151]
	v_cvt_pk_bf16_f32 v152, v164, v165
	v_cvt_pk_bf16_f32 v153, v162, v163
	global_store_dwordx2 v[158:159], v[152:153], off offset:256 sc1
	v_cvt_pk_bf16_f32 v148, v148, v149
	v_cvt_pk_bf16_f32 v149, v150, v151
	global_store_dwordx2 v[158:159], v[148:149], off offset:320 sc1
	global_load_dwordx4 v[148:151], v[160:161], off offset:2048
	v_lshl_add_u64 v[152:153], v[202:203], 0, v[156:157]
	global_load_dwordx4 v[152:155], v[152:153], off offset:2048
	v_lshl_add_u64 v[156:157], v[140:141], 3, s[6:7]
	v_mad_u64_u32 v[158:159], s[8:9], v156, s25, v[206:207]
	v_lshlrev_b32_e32 v156, 5, v147
	v_mad_i32_i24 v159, v157, s25, v159
	v_ashrrev_i32_e32 v157, 31, v156
	v_lshlrev_b64 v[156:157], 2, v[156:157]
	v_lshl_add_u64 v[160:161], v[204:205], 0, v[156:157]
	s_waitcnt vmcnt(1)
	v_pk_mul_f32 v[164:165], v[74:75], v[148:149]
	v_pk_mul_f32 v[148:149], v[78:79], v[148:149]
	v_pk_mul_f32 v[162:163], v[76:77], v[150:151]
	v_pk_mul_f32 v[150:151], v[80:81], v[150:151]
	s_waitcnt vmcnt(0)
	v_pk_fma_f32 v[148:149], v[74:75], v[152:153], v[148:149]
	v_pk_fma_f32 v[162:163], v[80:81], v[154:155], v[162:163] neg_lo:[0,0,1] neg_hi:[0,0,1]
	v_pk_fma_f32 v[164:165], v[78:79], v[152:153], v[164:165] neg_lo:[0,0,1] neg_hi:[0,0,1]
	v_pk_fma_f32 v[150:151], v[76:77], v[154:155], v[150:151]
	v_cvt_pk_bf16_f32 v152, v164, v165
	v_cvt_pk_bf16_f32 v153, v162, v163
	global_store_dwordx2 v[158:159], v[152:153], off offset:256 sc1
	v_cvt_pk_bf16_f32 v148, v148, v149
	v_cvt_pk_bf16_f32 v149, v150, v151
	global_store_dwordx2 v[158:159], v[148:149], off offset:320 sc1
	global_load_dwordx4 v[148:151], v[160:161], off offset:2048
	v_lshl_add_u64 v[152:153], v[202:203], 0, v[156:157]
	global_load_dwordx4 v[152:155], v[152:153], off offset:2048
	v_lshl_add_u64 v[156:157], v[138:139], 3, s[6:7]
	v_mad_u64_u32 v[158:159], s[8:9], v156, s25, v[206:207]
	v_mad_i32_i24 v159, v157, s25, v159
	s_mov_b64 s[8:9], 0
	s_waitcnt vmcnt(1)
	v_pk_mul_f32 v[160:161], v[66:67], v[148:149]
	v_pk_mul_f32 v[148:149], v[70:71], v[148:149]
	v_pk_mul_f32 v[156:157], v[68:69], v[150:151]
	v_pk_mul_f32 v[150:151], v[72:73], v[150:151]
	s_waitcnt vmcnt(0)
	v_pk_fma_f32 v[148:149], v[66:67], v[152:153], v[148:149]
	v_pk_fma_f32 v[156:157], v[72:73], v[154:155], v[156:157] neg_lo:[0,0,1] neg_hi:[0,0,1]
	v_pk_fma_f32 v[160:161], v[70:71], v[152:153], v[160:161] neg_lo:[0,0,1] neg_hi:[0,0,1]
	v_pk_fma_f32 v[150:151], v[68:69], v[154:155], v[150:151]
	v_cvt_pk_bf16_f32 v152, v160, v161
	v_cvt_pk_bf16_f32 v153, v156, v157
	global_store_dwordx2 v[158:159], v[152:153], off offset:256 sc1
	v_cvt_pk_bf16_f32 v148, v148, v149
	v_cvt_pk_bf16_f32 v149, v150, v151
	global_store_dwordx2 v[158:159], v[148:149], off offset:320 sc1
; __device__ __forceinline__ unsigned cvt_pk_bf16(float lo, float hi) { unsigned r; asm volatile("v_cvt_pk_bf16_f32 %0, %1, %2" : "=v"(r) : "v"(lo), "v"(hi)); return r; }
;     __device__ __forceinline__ void operator()(const f32x4 (&acc)[2][2][4][2], const Unit& u, int wr, int wc, int fr, int fq, const LAS float* bl) const {
;     ...
;             if (type < 2) {
;                 const int dim = 64 * type + 32 * blk + 8 * fq;
; #pragma unroll
;                 for (int ai = 0; ai < 2; ++ai)
; #pragma unroll
;                     for (int m = 0; m < 4; ++m) { const int r = row0 + ai * HALF + m * 16; const f32x4 v0 = acc[ai][bj][m][0], v1 = acc[ai][bj][m][1];
;                         u32x4 w; w.x = cvt_pk_bf16(v0[0], v0[1]); w.y = cvt_pk_bf16(v0[2], v0[3]); w.z = cvt_pk_bf16(v1[0], v1[1]); w.w = cvt_pk_bf16(v1[2], v1[3]);
;                         *(u32x4*)(Q + ((size_t)r * NH + head) * DQK + dim) = w; }
;             } else {
;                 const int i0 = 16 * blk + 4 * fq;
; #pragma unroll
;                 for (int ai = 0; ai < 2; ++ai)
; #pragma unroll
;                     for (int m = 0; m < 4; ++m) { const int r = row0 + ai * HALF + m * 16, pos = (r % S) + NMETA;
.LBB0_482:
	s_andn2_b64 vcc, exec, s[8:9]
	s_cbranch_vccnz .LBB0_484
	s_ashr_i32 s7, s6, 31
	v_lshl_or_b32 v148, s28, 6, v222
	v_cvt_pk_bf16_f32 v126, v126, v127
	v_cvt_pk_bf16_f32 v127, v128, v129
	v_cvt_pk_bf16_f32 v128, v122, v123
	v_cvt_pk_bf16_f32 v129, v124, v125
	v_lshl_add_u64 v[122:123], v[136:137], 3, s[6:7]
	v_mov_b64_e32 v[124:125], s[46:47]
	v_ashrrev_i32_e32 v149, 31, v148
	v_mad_u64_u32 v[150:151], s[8:9], v122, s25, v[124:125]
	v_mad_i32_i24 v151, v123, s25, v151
	v_lshlrev_b64 v[148:149], 1, v[148:149]
	v_lshl_add_u64 v[150:151], v[150:151], 0, v[148:149]
	global_store_dwordx4 v[150:151], v[126:129], off sc1
	v_cvt_pk_bf16_f32 v118, v118, v119
	v_cvt_pk_bf16_f32 v119, v120, v121
	v_cvt_pk_bf16_f32 v120, v114, v115
	v_lshl_add_u64 v[114:115], v[134:135], 3, s[6:7]
	v_cvt_pk_bf16_f32 v121, v116, v117
	v_mad_u64_u32 v[116:117], s[8:9], v114, s25, v[124:125]
	v_mad_i32_i24 v117, v115, s25, v117
	v_lshl_add_u64 v[114:115], v[116:117], 0, v[148:149]
	global_store_dwordx4 v[114:115], v[118:121], off sc1
	v_cvt_pk_bf16_f32 v110, v110, v111
	v_cvt_pk_bf16_f32 v111, v112, v113
	v_cvt_pk_bf16_f32 v112, v106, v107
	v_lshl_add_u64 v[106:107], v[132:133], 3, s[6:7]
	v_cvt_pk_bf16_f32 v113, v108, v109
	v_mad_u64_u32 v[108:109], s[8:9], v106, s25, v[124:125]
	v_mad_i32_i24 v109, v107, s25, v109
	v_lshl_add_u64 v[106:107], v[108:109], 0, v[148:149]
	global_store_dwordx4 v[106:107], v[110:113], off sc1
	v_cvt_pk_bf16_f32 v102, v102, v103
	v_cvt_pk_bf16_f32 v103, v104, v105
	v_cvt_pk_bf16_f32 v104, v98, v99
	v_lshl_add_u64 v[98:99], v[130:131], 3, s[6:7]
	v_cvt_pk_bf16_f32 v105, v100, v101
	v_mad_u64_u32 v[100:101], s[6:7], v98, s25, v[124:125]
	v_mad_i32_i24 v101, v99, s25, v101
	v_lshl_add_u64 v[98:99], v[100:101], 0, v[148:149]
	global_store_dwordx4 v[98:99], v[102:105], off sc1
	v_cvt_pk_bf16_f32 v94, v94, v95
	v_cvt_pk_bf16_f32 v95, v96, v97
	v_cvt_pk_bf16_f32 v96, v90, v91
	v_lshl_add_u64 v[90:91], v[122:123], 0, s[62:63]
	v_cvt_pk_bf16_f32 v97, v92, v93
	v_mad_u64_u32 v[92:93], s[6:7], v90, s25, v[124:125]
	v_mad_i32_i24 v93, v91, s25, v93
	v_lshl_add_u64 v[90:91], v[92:93], 0, v[148:149]
	global_store_dwordx4 v[90:91], v[94:97], off sc1
	v_cvt_pk_bf16_f32 v86, v86, v87
	v_cvt_pk_bf16_f32 v87, v88, v89
	v_cvt_pk_bf16_f32 v88, v82, v83
	v_lshl_add_u64 v[82:83], v[122:123], 0, s[64:65]
	v_cvt_pk_bf16_f32 v89, v84, v85
	v_mad_u64_u32 v[84:85], s[6:7], v82, s25, v[124:125]
	v_mad_i32_i24 v85, v83, s25, v85
	v_lshl_add_u64 v[82:83], v[84:85], 0, v[148:149]
	global_store_dwordx4 v[82:83], v[86:89], off sc1
	v_cvt_pk_bf16_f32 v78, v78, v79
	v_cvt_pk_bf16_f32 v79, v80, v81
	v_cvt_pk_bf16_f32 v80, v74, v75
	v_lshl_add_u64 v[74:75], v[122:123], 0, s[66:67]
	v_cvt_pk_bf16_f32 v81, v76, v77
	v_mad_u64_u32 v[76:77], s[6:7], v74, s25, v[124:125]
	v_mad_i32_i24 v77, v75, s25, v77
	v_lshl_add_u64 v[74:75], v[76:77], 0, v[148:149]
	global_store_dwordx4 v[74:75], v[78:81], off sc1
	v_cvt_pk_bf16_f32 v70, v70, v71
	v_cvt_pk_bf16_f32 v71, v72, v73
	v_cvt_pk_bf16_f32 v72, v66, v67
	v_lshl_add_u64 v[66:67], v[122:123], 0, s[68:69]
	v_cvt_pk_bf16_f32 v73, v68, v69
	v_mad_u64_u32 v[68:69], s[6:7], v66, s25, v[124:125]
	v_mad_i32_i24 v69, v67, s25, v69
	v_lshl_add_u64 v[66:67], v[68:69], 0, v[148:149]
	global_store_dwordx4 v[66:67], v[70:73], off sc1
.LBB0_484:
	s_or_b32 s7, s19, 2
	s_mul_hi_i32 s6, s7, 0x55555556
	s_lshr_b32 s8, s6, 31
	s_add_i32 s6, s6, s8
	s_mul_i32 s8, s6, 3
	s_sub_i32 s19, s7, s8
	s_cmp_lt_i32 s19, 2
	s_mov_b64 s[8:9], -1
	s_cbranch_scc1 .LBB0_487
	v_add_u32_e32 v66, v136, v146
	v_and_b32_e32 v66, 0x7fff000, v66
	v_sub_u32_e32 v66, v136, v66
	v_lshlrev_b32_e32 v66, 5, v66
	v_ashrrev_i32_e32 v67, 31, v66
	v_lshlrev_b64 v[70:71], 2, v[66:67]
	v_lshl_add_u64 v[66:67], v[204:205], 0, v[70:71]
	global_load_dwordx4 v[66:69], v[66:67], off offset:2048
	v_lshl_add_u64 v[70:71], v[202:203], 0, v[70:71]
	global_load_dwordx4 v[70:73], v[70:71], off offset:2048
	s_ashr_i32 s7, s6, 31
	v_add_u32_e32 v76, v134, v146
	v_lshl_add_u64 v[74:75], v[136:137], 3, s[6:7]
	v_and_b32_e32 v78, 0x7fff000, v76
	v_mad_u64_u32 v[76:77], s[8:9], v74, s25, v[206:207]
	v_sub_u32_e32 v74, v134, v78
	v_lshlrev_b32_e32 v74, 5, v74
	v_mad_i32_i24 v77, v75, s25, v77
	v_ashrrev_i32_e32 v75, 31, v74
	v_lshlrev_b64 v[74:75], 2, v[74:75]
	v_lshl_add_u64 v[78:79], v[204:205], 0, v[74:75]
	v_ashrrev_i32_e32 v139, 31, v138
	s_waitcnt vmcnt(0)
	v_pk_mul_f32 v[82:83], v[58:59], v[66:67]
	v_pk_mul_f32 v[66:67], v[62:63], v[66:67]
	v_pk_mul_f32 v[80:81], v[60:61], v[68:69]
	v_pk_mul_f32 v[68:69], v[64:65], v[68:69]
	v_pk_fma_f32 v[66:67], v[58:59], v[70:71], v[66:67]
	v_pk_fma_f32 v[80:81], v[64:65], v[72:73], v[80:81] neg_lo:[0,0,1] neg_hi:[0,0,1]
	v_pk_fma_f32 v[82:83], v[62:63], v[70:71], v[82:83] neg_lo:[0,0,1] neg_hi:[0,0,1]
	v_pk_fma_f32 v[68:69], v[60:61], v[72:73], v[68:69]
	v_cvt_pk_bf16_f32 v70, v82, v83
	v_cvt_pk_bf16_f32 v71, v80, v81
	global_store_dwordx2 v[76:77], v[70:71], off offset:256 sc1
	v_cvt_pk_bf16_f32 v66, v66, v67
	v_cvt_pk_bf16_f32 v67, v68, v69
	global_store_dwordx2 v[76:77], v[66:67], off offset:320 sc1
	global_load_dwordx4 v[66:69], v[78:79], off offset:2048
	v_lshl_add_u64 v[70:71], v[202:203], 0, v[74:75]
	global_load_dwordx4 v[70:73], v[70:71], off offset:2048
	v_add_u32_e32 v76, v132, v146
	v_lshl_add_u64 v[74:75], v[134:135], 3, s[6:7]
	v_and_b32_e32 v78, 0x7fff000, v76
	v_mad_u64_u32 v[76:77], s[8:9], v74, s25, v[206:207]
	v_sub_u32_e32 v74, v132, v78
	v_lshlrev_b32_e32 v74, 5, v74
	v_mad_i32_i24 v77, v75, s25, v77
	v_ashrrev_i32_e32 v75, 31, v74
	v_lshlrev_b64 v[74:75], 2, v[74:75]
	v_lshl_add_u64 v[78:79], v[204:205], 0, v[74:75]
	s_waitcnt vmcnt(0)
; __device__ __forceinline__ unsigned cvt_pk_bf16(float lo, float hi) { unsigned r; asm volatile("v_cvt_pk_bf16_f32 %0, %1, %2" : "=v"(r) : "v"(lo), "v"(hi)); return r; }
;     __device__ __forceinline__ void operator()(const f32x4 (&acc)[2][2][4][2], const Unit& u, int wr, int wc, int fr, int fq, const LAS float* bl) const {
;     ...
;                     for (int m = 0; m < 4; ++m) { const int r = row0 + ai * HALF + m * 16, pos = (r % S) + NMETA;
;                         const f32x4 cs = *(const f32x4*)(cosT + pos * 32 + i0), sn = *(const f32x4*)(sinT + pos * 32 + i0);
;                         const f32x4 x1 = acc[ai][bj][m][0], x2 = acc[ai][bj][m][1];
;                         const f32x4 o1 = x1 * cs - x2 * sn, o2 = x1 * sn + x2 * cs;
;                         bf16* dst = Q + ((size_t)r * NH + head) * DQK + 128 + i0;
;                         u32x2 w1; w1.x = cvt_pk_bf16(o1[0], o1[1]); w1.y = cvt_pk_bf16(o1[2], o1[3]); *(u32x2*)(dst) = w1;
;                         u32x2 w2; w2.x = cvt_pk_bf16(o2[0], o2[1]); w2.y = cvt_pk_bf16(o2[2], o2[3]); *(u32x2*)(dst + 32) = w2; }
	v_pk_mul_f32 v[82:83], v[50:51], v[66:67]
	v_pk_mul_f32 v[66:67], v[54:55], v[66:67]
	v_pk_mul_f32 v[80:81], v[52:53], v[68:69]
	v_pk_mul_f32 v[68:69], v[56:57], v[68:69]
	v_pk_fma_f32 v[66:67], v[50:51], v[70:71], v[66:67]
	v_pk_fma_f32 v[80:81], v[56:57], v[72:73], v[80:81] neg_lo:[0,0,1] neg_hi:[0,0,1]
	v_pk_fma_f32 v[82:83], v[54:55], v[70:71], v[82:83] neg_lo:[0,0,1] neg_hi:[0,0,1]
	v_pk_fma_f32 v[68:69], v[52:53], v[72:73], v[68:69]
	v_cvt_pk_bf16_f32 v70, v82, v83
	v_cvt_pk_bf16_f32 v71, v80, v81
	global_store_dwordx2 v[76:77], v[70:71], off offset:256 sc1
	v_cvt_pk_bf16_f32 v66, v66, v67
	v_cvt_pk_bf16_f32 v67, v68, v69
	global_store_dwordx2 v[76:77], v[66:67], off offset:320 sc1
	global_load_dwordx4 v[66:69], v[78:79], off offset:2048
	v_lshl_add_u64 v[70:71], v[202:203], 0, v[74:75]
	global_load_dwordx4 v[70:73], v[70:71], off offset:2048
	v_add_u32_e32 v76, v130, v146
	v_lshl_add_u64 v[74:75], v[132:133], 3, s[6:7]
	v_and_b32_e32 v78, 0x7fff000, v76
	v_mad_u64_u32 v[76:77], s[8:9], v74, s25, v[206:207]
	v_sub_u32_e32 v74, v130, v78
	v_lshlrev_b32_e32 v74, 5, v74
	v_mad_i32_i24 v77, v75, s25, v77
	v_ashrrev_i32_e32 v75, 31, v74
	v_lshlrev_b64 v[74:75], 2, v[74:75]
	v_lshl_add_u64 v[78:79], v[204:205], 0, v[74:75]
	s_waitcnt vmcnt(0)
	v_pk_mul_f32 v[82:83], v[42:43], v[66:67]
	v_pk_mul_f32 v[66:67], v[46:47], v[66:67]
	v_pk_mul_f32 v[80:81], v[44:45], v[68:69]
	v_pk_mul_f32 v[68:69], v[48:49], v[68:69]
	v_pk_fma_f32 v[66:67], v[42:43], v[70:71], v[66:67]
	v_pk_fma_f32 v[80:81], v[48:49], v[72:73], v[80:81] neg_lo:[0,0,1] neg_hi:[0,0,1]
	v_pk_fma_f32 v[82:83], v[46:47], v[70:71], v[82:83] neg_lo:[0,0,1] neg_hi:[0,0,1]
	v_pk_fma_f32 v[68:69], v[44:45], v[72:73], v[68:69]
	v_cvt_pk_bf16_f32 v70, v82, v83
	v_cvt_pk_bf16_f32 v71, v80, v81
	global_store_dwordx2 v[76:77], v[70:71], off offset:256 sc1
	v_cvt_pk_bf16_f32 v66, v66, v67
	v_cvt_pk_bf16_f32 v67, v68, v69
	global_store_dwordx2 v[76:77], v[66:67], off offset:320 sc1
	global_load_dwordx4 v[66:69], v[78:79], off offset:2048
	v_lshl_add_u64 v[70:71], v[202:203], 0, v[74:75]
	global_load_dwordx4 v[70:73], v[70:71], off offset:2048
	v_lshrrev_b32_e32 v76, 20, v145
	v_lshl_add_u64 v[74:75], v[130:131], 3, s[6:7]
	v_add_u32_e32 v78, v144, v76
	v_mad_u64_u32 v[76:77], s[8:9], v74, s25, v[206:207]
	v_and_b32_e32 v74, 0x7fff000, v78
	v_sub_u32_e32 v74, v144, v74
	v_lshlrev_b32_e32 v74, 5, v74
	v_mad_i32_i24 v77, v75, s25, v77
	v_ashrrev_i32_e32 v75, 31, v74
	v_lshlrev_b64 v[74:75], 2, v[74:75]
	v_lshl_add_u64 v[78:79], v[204:205], 0, v[74:75]
	s_waitcnt vmcnt(0)
	v_pk_mul_f32 v[82:83], v[34:35], v[66:67]
	v_pk_mul_f32 v[66:67], v[38:39], v[66:67]
	v_pk_mul_f32 v[80:81], v[36:37], v[68:69]
	v_pk_mul_f32 v[68:69], v[40:41], v[68:69]
	v_pk_fma_f32 v[66:67], v[34:35], v[70:71], v[66:67]
	v_pk_fma_f32 v[80:81], v[40:41], v[72:73], v[80:81] neg_lo:[0,0,1] neg_hi:[0,0,1]
	v_pk_fma_f32 v[82:83], v[38:39], v[70:71], v[82:83] neg_lo:[0,0,1] neg_hi:[0,0,1]
	v_pk_fma_f32 v[68:69], v[36:37], v[72:73], v[68:69]
	v_cvt_pk_bf16_f32 v70, v82, v83
	v_cvt_pk_bf16_f32 v71, v80, v81
	global_store_dwordx2 v[76:77], v[70:71], off offset:256 sc1
	v_cvt_pk_bf16_f32 v66, v66, v67
	v_cvt_pk_bf16_f32 v67, v68, v69
	global_store_dwordx2 v[76:77], v[66:67], off offset:320 sc1
	global_load_dwordx4 v[66:69], v[78:79], off offset:2048
	v_lshl_add_u64 v[70:71], v[202:203], 0, v[74:75]
	global_load_dwordx4 v[70:73], v[70:71], off offset:2048
	v_lshrrev_b32_e32 v76, 20, v143
	v_lshl_add_u64 v[74:75], v[144:145], 3, s[6:7]
	v_add_u32_e32 v78, v142, v76
	v_mad_u64_u32 v[76:77], s[8:9], v74, s25, v[206:207]
	v_and_b32_e32 v74, 0x7fff000, v78
	v_sub_u32_e32 v74, v142, v74
	v_lshlrev_b32_e32 v74, 5, v74
	v_mad_i32_i24 v77, v75, s25, v77
	v_ashrrev_i32_e32 v75, 31, v74
	v_lshlrev_b64 v[74:75], 2, v[74:75]
	v_lshl_add_u64 v[78:79], v[204:205], 0, v[74:75]
	s_waitcnt vmcnt(0)
; __device__ __forceinline__ unsigned cvt_pk_bf16(float lo, float hi) { unsigned r; asm volatile("v_cvt_pk_bf16_f32 %0, %1, %2" : "=v"(r) : "v"(lo), "v"(hi)); return r; }
;     __device__ __forceinline__ void operator()(const f32x4 (&acc)[2][2][4][2], const Unit& u, int wr, int wc, int fr, int fq, const LAS float* bl) const {
;     ...
;                     for (int m = 0; m < 4; ++m) { const int r = row0 + ai * HALF + m * 16, pos = (r % S) + NMETA;
;                         const f32x4 cs = *(const f32x4*)(cosT + pos * 32 + i0), sn = *(const f32x4*)(sinT + pos * 32 + i0);
;                         const f32x4 x1 = acc[ai][bj][m][0], x2 = acc[ai][bj][m][1];
;                         const f32x4 o1 = x1 * cs - x2 * sn, o2 = x1 * sn + x2 * cs;
;                         bf16* dst = Q + ((size_t)r * NH + head) * DQK + 128 + i0;
;                         u32x2 w1; w1.x = cvt_pk_bf16(o1[0], o1[1]); w1.y = cvt_pk_bf16(o1[2], o1[3]); *(u32x2*)(dst) = w1;
;                         u32x2 w2; w2.x = cvt_pk_bf16(o2[0], o2[1]); w2.y = cvt_pk_bf16(o2[2], o2[3]); *(u32x2*)(dst + 32) = w2; }
	v_pk_mul_f32 v[82:83], v[26:27], v[66:67]
	v_pk_mul_f32 v[66:67], v[30:31], v[66:67]
	v_pk_mul_f32 v[80:81], v[28:29], v[68:69]
	v_pk_mul_f32 v[68:69], v[32:33], v[68:69]
	v_pk_fma_f32 v[66:67], v[26:27], v[70:71], v[66:67]
	v_pk_fma_f32 v[80:81], v[32:33], v[72:73], v[80:81] neg_lo:[0,0,1] neg_hi:[0,0,1]
	v_pk_fma_f32 v[82:83], v[30:31], v[70:71], v[82:83] neg_lo:[0,0,1] neg_hi:[0,0,1]
	v_pk_fma_f32 v[68:69], v[28:29], v[72:73], v[68:69]
	v_cvt_pk_bf16_f32 v70, v82, v83
	v_cvt_pk_bf16_f32 v71, v80, v81
	global_store_dwordx2 v[76:77], v[70:71], off offset:256 sc1
	v_cvt_pk_bf16_f32 v66, v66, v67
	v_cvt_pk_bf16_f32 v67, v68, v69
	global_store_dwordx2 v[76:77], v[66:67], off offset:320 sc1
	global_load_dwordx4 v[66:69], v[78:79], off offset:2048
	v_lshl_add_u64 v[70:71], v[202:203], 0, v[74:75]
	global_load_dwordx4 v[70:73], v[70:71], off offset:2048
	v_lshrrev_b32_e32 v76, 20, v141
	v_lshl_add_u64 v[74:75], v[142:143], 3, s[6:7]
	v_add_u32_e32 v78, v140, v76
	v_mad_u64_u32 v[76:77], s[8:9], v74, s25, v[206:207]
	v_and_b32_e32 v74, 0x7fff000, v78
	v_sub_u32_e32 v74, v140, v74
	v_lshlrev_b32_e32 v74, 5, v74
	v_mad_i32_i24 v77, v75, s25, v77
	v_ashrrev_i32_e32 v75, 31, v74
	v_lshlrev_b64 v[74:75], 2, v[74:75]
	v_lshl_add_u64 v[78:79], v[204:205], 0, v[74:75]
	s_waitcnt vmcnt(0)
	v_pk_mul_f32 v[82:83], v[6:7], v[66:67]
	v_pk_mul_f32 v[66:67], v[14:15], v[66:67]
	v_pk_mul_f32 v[80:81], v[8:9], v[68:69]
	v_pk_mul_f32 v[68:69], v[16:17], v[68:69]
	v_pk_fma_f32 v[66:67], v[6:7], v[70:71], v[66:67]
	v_pk_fma_f32 v[80:81], v[16:17], v[72:73], v[80:81] neg_lo:[0,0,1] neg_hi:[0,0,1]
	v_pk_fma_f32 v[82:83], v[14:15], v[70:71], v[82:83] neg_lo:[0,0,1] neg_hi:[0,0,1]
	v_pk_fma_f32 v[68:69], v[8:9], v[72:73], v[68:69]
	v_cvt_pk_bf16_f32 v70, v82, v83
	v_cvt_pk_bf16_f32 v71, v80, v81
	global_store_dwordx2 v[76:77], v[70:71], off offset:256 sc1
	v_cvt_pk_bf16_f32 v66, v66, v67
	v_cvt_pk_bf16_f32 v67, v68, v69
	global_store_dwordx2 v[76:77], v[66:67], off offset:320 sc1
	global_load_dwordx4 v[66:69], v[78:79], off offset:2048
	v_lshl_add_u64 v[70:71], v[202:203], 0, v[74:75]
	global_load_dwordx4 v[70:73], v[70:71], off offset:2048
	v_lshl_add_u64 v[74:75], v[140:141], 3, s[6:7]
	v_lshrrev_b32_e32 v78, 20, v139
	v_mad_u64_u32 v[76:77], s[8:9], v74, s25, v[206:207]
	v_add_u32_e32 v74, v138, v78
	v_and_b32_e32 v74, 0x7fff000, v74
	v_sub_u32_e32 v74, v138, v74
	v_lshlrev_b32_e32 v74, 5, v74
	v_mad_i32_i24 v77, v75, s25, v77
	v_ashrrev_i32_e32 v75, 31, v74
	v_lshlrev_b64 v[74:75], 2, v[74:75]
	v_lshl_add_u64 v[78:79], v[204:205], 0, v[74:75]
	s_waitcnt vmcnt(0)
	v_pk_mul_f32 v[82:83], v[18:19], v[66:67]
	v_pk_mul_f32 v[66:67], v[22:23], v[66:67]
	v_pk_mul_f32 v[80:81], v[20:21], v[68:69]
	v_pk_mul_f32 v[68:69], v[24:25], v[68:69]
	v_pk_fma_f32 v[66:67], v[18:19], v[70:71], v[66:67]
	v_pk_fma_f32 v[80:81], v[24:25], v[72:73], v[80:81] neg_lo:[0,0,1] neg_hi:[0,0,1]
	v_pk_fma_f32 v[82:83], v[22:23], v[70:71], v[82:83] neg_lo:[0,0,1] neg_hi:[0,0,1]
	v_pk_fma_f32 v[68:69], v[20:21], v[72:73], v[68:69]
	v_cvt_pk_bf16_f32 v70, v82, v83
	v_cvt_pk_bf16_f32 v71, v80, v81
	global_store_dwordx2 v[76:77], v[70:71], off offset:256 sc1
	v_cvt_pk_bf16_f32 v66, v66, v67
	v_cvt_pk_bf16_f32 v67, v68, v69
	global_store_dwordx2 v[76:77], v[66:67], off offset:320 sc1
	global_load_dwordx4 v[66:69], v[78:79], off offset:2048
	v_lshl_add_u64 v[70:71], v[202:203], 0, v[74:75]
	global_load_dwordx4 v[70:73], v[70:71], off offset:2048
	v_lshl_add_u64 v[74:75], v[138:139], 3, s[6:7]
	v_mad_u64_u32 v[76:77], s[8:9], v74, s25, v[206:207]
	v_mad_i32_i24 v77, v75, s25, v77
	s_waitcnt vmcnt(0)
	v_pk_mul_f32 v[78:79], v[2:3], v[66:67]
	v_pk_mul_f32 v[66:67], v[10:11], v[66:67]
	v_pk_mul_f32 v[74:75], v[4:5], v[68:69]
	v_pk_mul_f32 v[68:69], v[12:13], v[68:69]
	v_pk_fma_f32 v[66:67], v[2:3], v[70:71], v[66:67]
	v_pk_fma_f32 v[74:75], v[12:13], v[72:73], v[74:75] neg_lo:[0,0,1] neg_hi:[0,0,1]
	v_pk_fma_f32 v[78:79], v[10:11], v[70:71], v[78:79] neg_lo:[0,0,1] neg_hi:[0,0,1]
	v_pk_fma_f32 v[68:69], v[4:5], v[72:73], v[68:69]
	v_cvt_pk_bf16_f32 v70, v78, v79
	v_cvt_pk_bf16_f32 v71, v74, v75
	global_store_dwordx2 v[76:77], v[70:71], off offset:256 sc1
	v_cvt_pk_bf16_f32 v66, v66, v67
	v_cvt_pk_bf16_f32 v67, v68, v69
	global_store_dwordx2 v[76:77], v[66:67], off offset:320 sc1
	s_cbranch_execz .LBB0_488

; __device__ __forceinline__ unsigned cvt_pk_bf16(float lo, float hi) { unsigned r; asm volatile("v_cvt_pk_bf16_f32 %0, %1, %2" : "=v"(r) : "v"(lo), "v"(hi)); return r; }
;     __device__ __forceinline__ void operator()(const f32x4 (&acc)[2][2][4][2], const Unit& u, int wr, int wc, int fr, int fq, const LAS float* bl) const {
;     ...
;             if (type < 2) {
;                 const int dim = 64 * type + 32 * blk + 8 * fq;
; #pragma unroll
;                 for (int ai = 0; ai < 2; ++ai)
; #pragma unroll
;                     for (int m = 0; m < 4; ++m) { const int r = row0 + ai * HALF + m * 16; const f32x4 v0 = acc[ai][bj][m][0], v1 = acc[ai][bj][m][1];
;                         u32x4 w; w.x = cvt_pk_bf16(v0[0], v0[1]); w.y = cvt_pk_bf16(v0[2], v0[3]); w.z = cvt_pk_bf16(v1[0], v1[1]); w.w = cvt_pk_bf16(v1[2], v1[3]);
;                         *(u32x4*)(Q + ((size_t)r * NH + head) * DQK + dim) = w; }
.LBB0_488:
	s_ashr_i32 s7, s6, 31
	v_lshl_or_b32 v66, s19, 6, v222
	v_cvt_pk_bf16_f32 v62, v62, v63
	v_cvt_pk_bf16_f32 v63, v64, v65
	v_cvt_pk_bf16_f32 v64, v58, v59
	v_cvt_pk_bf16_f32 v65, v60, v61
	v_lshl_add_u64 v[58:59], v[136:137], 3, s[6:7]
	v_mov_b64_e32 v[60:61], s[46:47]
	v_ashrrev_i32_e32 v67, 31, v66
	v_mad_u64_u32 v[68:69], s[8:9], v58, s25, v[60:61]
	v_mad_i32_i24 v69, v59, s25, v69
	v_lshlrev_b64 v[66:67], 1, v[66:67]
	v_lshl_add_u64 v[68:69], v[68:69], 0, v[66:67]
	global_store_dwordx4 v[68:69], v[62:65], off sc1
	v_cvt_pk_bf16_f32 v54, v54, v55
	v_cvt_pk_bf16_f32 v55, v56, v57
	v_cvt_pk_bf16_f32 v56, v50, v51
	v_lshl_add_u64 v[50:51], v[134:135], 3, s[6:7]
	v_cvt_pk_bf16_f32 v57, v52, v53
	v_mad_u64_u32 v[52:53], s[8:9], v50, s25, v[60:61]
	v_mad_i32_i24 v53, v51, s25, v53
	v_lshl_add_u64 v[50:51], v[52:53], 0, v[66:67]
	global_store_dwordx4 v[50:51], v[54:57], off sc1
	v_cvt_pk_bf16_f32 v46, v46, v47
	v_cvt_pk_bf16_f32 v47, v48, v49
	v_cvt_pk_bf16_f32 v48, v42, v43
	v_lshl_add_u64 v[42:43], v[132:133], 3, s[6:7]
	v_cvt_pk_bf16_f32 v49, v44, v45
	v_mad_u64_u32 v[44:45], s[8:9], v42, s25, v[60:61]
	v_mad_i32_i24 v45, v43, s25, v45
	v_lshl_add_u64 v[42:43], v[44:45], 0, v[66:67]
	global_store_dwordx4 v[42:43], v[46:49], off sc1
	v_cvt_pk_bf16_f32 v38, v38, v39
	v_cvt_pk_bf16_f32 v39, v40, v41
	v_cvt_pk_bf16_f32 v40, v34, v35
	v_lshl_add_u64 v[34:35], v[130:131], 3, s[6:7]
	v_cvt_pk_bf16_f32 v41, v36, v37
	v_mad_u64_u32 v[36:37], s[6:7], v34, s25, v[60:61]
	v_mad_i32_i24 v37, v35, s25, v37
	v_lshl_add_u64 v[34:35], v[36:37], 0, v[66:67]
	global_store_dwordx4 v[34:35], v[38:41], off sc1
	v_cvt_pk_bf16_f32 v30, v30, v31
	v_cvt_pk_bf16_f32 v31, v32, v33
	v_cvt_pk_bf16_f32 v32, v26, v27
	v_lshl_add_u64 v[26:27], v[58:59], 0, s[62:63]
	v_cvt_pk_bf16_f32 v33, v28, v29
	v_mad_u64_u32 v[28:29], s[6:7], v26, s25, v[60:61]
	v_mad_i32_i24 v29, v27, s25, v29
	v_lshl_add_u64 v[26:27], v[28:29], 0, v[66:67]
	global_store_dwordx4 v[26:27], v[30:33], off sc1
	v_cvt_pk_bf16_f32 v14, v14, v15
	v_cvt_pk_bf16_f32 v15, v16, v17
	v_cvt_pk_bf16_f32 v16, v6, v7
	v_lshl_add_u64 v[6:7], v[58:59], 0, s[64:65]
	v_cvt_pk_bf16_f32 v17, v8, v9
	v_mad_u64_u32 v[8:9], s[6:7], v6, s25, v[60:61]
	v_mad_i32_i24 v9, v7, s25, v9
	v_lshl_add_u64 v[6:7], v[8:9], 0, v[66:67]
	global_store_dwordx4 v[6:7], v[14:17], off sc1
	v_cvt_pk_bf16_f32 v6, v22, v23
	v_cvt_pk_bf16_f32 v7, v24, v25
	v_cvt_pk_bf16_f32 v8, v18, v19
	v_cvt_pk_bf16_f32 v9, v20, v21
	s_nop 1
	v_lshl_add_u64 v[14:15], v[58:59], 0, s[66:67]
	v_mad_u64_u32 v[16:17], s[6:7], v14, s25, v[60:61]
	v_mad_i32_i24 v17, v15, s25, v17
	v_lshl_add_u64 v[14:15], v[16:17], 0, v[66:67]
	global_store_dwordx4 v[14:15], v[6:9], off sc1
	s_nop 1
	v_cvt_pk_bf16_f32 v6, v10, v11
	v_cvt_pk_bf16_f32 v7, v12, v13
	v_cvt_pk_bf16_f32 v8, v2, v3
	v_lshl_add_u64 v[2:3], v[58:59], 0, s[68:69]
	v_cvt_pk_bf16_f32 v9, v4, v5
	v_mad_u64_u32 v[4:5], s[6:7], v2, s25, v[60:61]
	v_mad_i32_i24 v5, v3, s25, v5
	v_lshl_add_u64 v[2:3], v[4:5], 0, v[66:67]
	global_store_dwordx4 v[2:3], v[6:9], off sc1
	s_andn2_b64 vcc, exec, s[4:5]
	s_mov_b64 s[4:5], -1
	s_cbranch_vccnz .LBB0_463

; #define LAS __attribute__((address_space(3)))
; __device__ __forceinline__ unsigned cvt_pk_bf16(float lo, float hi) { unsigned r; asm volatile("v_cvt_pk_bf16_f32 %0, %1, %2" : "=v"(r) : "v"(lo), "v"(hi)); return r; }
;     __device__ void operator()(int r, int n, float v) const { if (r < NMETA) proj[(size_t)(M + r) * DINP + n] = f2bf(v); }
;     __device__ __forceinline__ void operator()(const f32x4 (&acc)[2][2][4][2], const Unit& u, int wr, int wc, int fr, int fq, const LAS float* bl) const {
;         const int row0 = u.pm * BM + wr * 64 + fr, col0 = u.pn * BM + wc * 32 + 8 * fq;
; #pragma unroll
;         for (int ai = 0; ai < 2; ++ai)
; #pragma unroll
;             for (int m = 0; m < 4; ++m) { const int r = row0 + ai * HALF + m * 16, b = r / S, pos = (r % S) + NMETA; bf16* rowp = kn + (size_t)(b * LP + pos) * (NH * 128) + col0;
; #pragma unroll
;                 for (int bj = 0; bj < 2; ++bj) { const f32x4 v0 = acc[ai][bj][m][0], v1 = acc[ai][bj][m][1];
;                     u32x4 w; w.x = cvt_pk_bf16(v0[0], v0[1]); w.y = cvt_pk_bf16(v0[2], v0[3]); w.z = cvt_pk_bf16(v1[0], v1[1]); w.w = cvt_pk_bf16(v1[2], v1[3]);
;                     *(u32x4*)(rowp + bj * HALF) = w; } }
;     }
.LBB0_524:
	v_lshl_add_u32 v134, s81, 8, v217
	v_ashrrev_i32_e32 v132, 31, v134
	v_lshrrev_b32_e32 v135, 20, v132
	v_add_u32_e32 v132, v134, v135
	v_ashrrev_i32_e32 v132, 12, v132
	v_mul_i32_i24_e32 v133, 0x1000, v132
	v_sub_u32_e32 v133, v134, v133
	v_mul_i32_i24_e32 v132, 0x1080, v132
	v_add3_u32 v132, v132, v133, 16
	v_lshl_or_b32 v130, s64, 8, v218
	v_ashrrev_i32_e32 v133, 31, v132
	v_ashrrev_i32_e32 v131, 31, v130
	v_lshlrev_b64 v[132:133], 11, v[132:133]
	v_lshl_add_u64 v[132:133], s[36:37], 0, v[132:133]
	v_lshlrev_b64 v[130:131], 1, v[130:131]
	v_lshl_add_u64 v[132:133], v[132:133], 0, v[130:131]
	v_cvt_pk_bf16_f32 v126, v126, v127
	v_cvt_pk_bf16_f32 v127, v128, v129
	v_cvt_pk_bf16_f32 v128, v122, v123
	v_cvt_pk_bf16_f32 v129, v124, v125
	global_store_dwordx4 v[132:133], v[126:129], off sc1
	v_cvt_pk_bf16_f32 v118, v118, v119
	v_cvt_pk_bf16_f32 v119, v120, v121
	v_cvt_pk_bf16_f32 v120, v114, v115
	v_or_b32_e32 v114, 16, v134
	v_add_u32_e32 v115, v114, v135
	v_ashrrev_i32_e32 v115, 12, v115
	v_cvt_pk_bf16_f32 v121, v116, v117
	v_mul_i32_i24_e32 v116, 0x1000, v115
	v_sub_u32_e32 v114, v114, v116
	v_mul_i32_i24_e32 v115, 0x1080, v115
	v_add3_u32 v114, v114, v115, 16
	v_ashrrev_i32_e32 v115, 31, v114
	v_lshlrev_b64 v[114:115], 11, v[114:115]
	v_lshl_add_u64 v[114:115], s[36:37], 0, v[114:115]
	v_lshl_add_u64 v[114:115], v[114:115], 0, v[130:131]
	global_store_dwordx4 v[132:133], v[118:121], off offset:256 sc1
	v_cvt_pk_bf16_f32 v110, v110, v111
	v_cvt_pk_bf16_f32 v111, v112, v113
	v_cvt_pk_bf16_f32 v112, v106, v107
	v_cvt_pk_bf16_f32 v113, v108, v109
	global_store_dwordx4 v[114:115], v[110:113], off sc1
	v_cvt_pk_bf16_f32 v102, v102, v103
	v_cvt_pk_bf16_f32 v103, v104, v105
	v_cvt_pk_bf16_f32 v104, v98, v99
	v_or_b32_e32 v98, 32, v134
	v_add_u32_e32 v99, v98, v135
	v_ashrrev_i32_e32 v99, 12, v99
	v_cvt_pk_bf16_f32 v105, v100, v101
	v_mul_i32_i24_e32 v100, 0x1000, v99
	v_sub_u32_e32 v98, v98, v100
	v_mul_i32_i24_e32 v99, 0x1080, v99
	v_add3_u32 v98, v99, v98, 16
	v_ashrrev_i32_e32 v99, 31, v98
	v_lshlrev_b64 v[98:99], 11, v[98:99]
	v_lshl_add_u64 v[98:99], s[36:37], 0, v[98:99]
	v_lshl_add_u64 v[98:99], v[98:99], 0, v[130:131]
	global_store_dwordx4 v[114:115], v[102:105], off offset:256 sc1
	v_cvt_pk_bf16_f32 v94, v94, v95
	v_cvt_pk_bf16_f32 v95, v96, v97
	v_cvt_pk_bf16_f32 v96, v90, v91
	v_cvt_pk_bf16_f32 v97, v92, v93
	global_store_dwordx4 v[98:99], v[94:97], off sc1
	v_cvt_pk_bf16_f32 v86, v86, v87
	v_cvt_pk_bf16_f32 v87, v88, v89
	v_cvt_pk_bf16_f32 v88, v82, v83
	v_or_b32_e32 v82, 48, v134
	v_add_u32_e32 v83, v82, v135
	v_ashrrev_i32_e32 v83, 12, v83
	v_cvt_pk_bf16_f32 v89, v84, v85
	v_mul_i32_i24_e32 v84, 0x1000, v83
	v_sub_u32_e32 v82, v82, v84
	v_mul_i32_i24_e32 v83, 0x1080, v83
	v_add3_u32 v82, v82, v83, 16
	v_ashrrev_i32_e32 v83, 31, v82
	v_lshlrev_b64 v[82:83], 11, v[82:83]
	v_lshl_add_u64 v[82:83], s[36:37], 0, v[82:83]
	v_lshl_add_u64 v[82:83], v[82:83], 0, v[130:131]
	global_store_dwordx4 v[98:99], v[86:89], off offset:256 sc1
	v_cvt_pk_bf16_f32 v78, v78, v79
	v_cvt_pk_bf16_f32 v79, v80, v81
	v_cvt_pk_bf16_f32 v80, v74, v75
	v_cvt_pk_bf16_f32 v81, v76, v77
	global_store_dwordx4 v[82:83], v[78:81], off sc1
	v_cvt_pk_bf16_f32 v70, v70, v71
	v_cvt_pk_bf16_f32 v71, v72, v73
	v_cvt_pk_bf16_f32 v72, v66, v67
	v_add_u32_e32 v66, 0x80, v134
	v_ashrrev_i32_e32 v67, 31, v66
	v_lshrrev_b32_e32 v67, 20, v67
	v_add_u32_e32 v67, v66, v67
	v_ashrrev_i32_e32 v67, 12, v67
	v_cvt_pk_bf16_f32 v73, v68, v69
	v_mul_i32_i24_e32 v68, 0x1000, v67
	v_sub_u32_e32 v66, v66, v68
	v_mul_i32_i24_e32 v67, 0x1080, v67
	v_add3_u32 v66, v67, v66, 16
	v_ashrrev_i32_e32 v67, 31, v66
	v_lshlrev_b64 v[66:67], 11, v[66:67]
	v_lshl_add_u64 v[66:67], s[36:37], 0, v[66:67]
	v_lshl_add_u64 v[66:67], v[66:67], 0, v[130:131]
	global_store_dwordx4 v[82:83], v[70:73], off offset:256 sc1
	v_cvt_pk_bf16_f32 v62, v62, v63
	v_cvt_pk_bf16_f32 v63, v64, v65
	v_cvt_pk_bf16_f32 v64, v58, v59
	v_cvt_pk_bf16_f32 v65, v60, v61
	global_store_dwordx4 v[66:67], v[62:65], off sc1
	v_cvt_pk_bf16_f32 v54, v54, v55
	v_cvt_pk_bf16_f32 v55, v56, v57
	v_cvt_pk_bf16_f32 v56, v50, v51
	v_add_u32_e32 v50, 0x90, v134
	v_ashrrev_i32_e32 v51, 31, v50
	v_lshrrev_b32_e32 v51, 20, v51
	v_add_u32_e32 v51, v50, v51
	v_ashrrev_i32_e32 v51, 12, v51
	v_cvt_pk_bf16_f32 v57, v52, v53
	v_mul_i32_i24_e32 v52, 0x1000, v51
	v_sub_u32_e32 v50, v50, v52
	v_mul_i32_i24_e32 v51, 0x1080, v51
	v_add3_u32 v50, v50, v51, 16
	v_ashrrev_i32_e32 v51, 31, v50
	v_lshlrev_b64 v[50:51], 11, v[50:51]
	v_lshl_add_u64 v[50:51], s[36:37], 0, v[50:51]
	v_lshl_add_u64 v[50:51], v[50:51], 0, v[130:131]
	global_store_dwordx4 v[66:67], v[54:57], off offset:256 sc1
	v_cvt_pk_bf16_f32 v46, v46, v47
	v_cvt_pk_bf16_f32 v47, v48, v49
	v_cvt_pk_bf16_f32 v48, v42, v43
	v_cvt_pk_bf16_f32 v49, v44, v45
	global_store_dwordx4 v[50:51], v[46:49], off sc1
	v_cvt_pk_bf16_f32 v38, v38, v39
	v_cvt_pk_bf16_f32 v39, v40, v41
	v_cvt_pk_bf16_f32 v40, v34, v35
	v_add_u32_e32 v34, 0xa0, v134
	v_ashrrev_i32_e32 v35, 31, v34
	v_lshrrev_b32_e32 v35, 20, v35
	v_add_u32_e32 v35, v34, v35
	v_ashrrev_i32_e32 v35, 12, v35
	v_cvt_pk_bf16_f32 v41, v36, v37
	v_mul_i32_i24_e32 v36, 0x1000, v35
	v_sub_u32_e32 v34, v34, v36
	v_mul_i32_i24_e32 v35, 0x1080, v35
	v_add3_u32 v34, v35, v34, 16
	v_ashrrev_i32_e32 v35, 31, v34
	v_lshlrev_b64 v[34:35], 11, v[34:35]
	v_lshl_add_u64 v[34:35], s[36:37], 0, v[34:35]
	v_lshl_add_u64 v[34:35], v[34:35], 0, v[130:131]
	global_store_dwordx4 v[50:51], v[38:41], off offset:256 sc1
	v_cvt_pk_bf16_f32 v22, v22, v23
	v_cvt_pk_bf16_f32 v23, v24, v25
	v_cvt_pk_bf16_f32 v24, v18, v19
	v_cvt_pk_bf16_f32 v25, v20, v21
	global_store_dwordx4 v[34:35], v[22:25], off sc1
	v_cvt_pk_bf16_f32 v18, v30, v31
	v_cvt_pk_bf16_f32 v19, v32, v33
	v_cvt_pk_bf16_f32 v20, v26, v27
	v_cvt_pk_bf16_f32 v21, v28, v29
	global_store_dwordx4 v[34:35], v[18:21], off offset:256 sc1
	s_andn2_b64 vcc, exec, s[4:5]
	s_mov_b64 s[4:5], -1
	v_add_u32_e32 v18, 0xb0, v134
	v_ashrrev_i32_e32 v19, 31, v18
	v_lshrrev_b32_e32 v19, 20, v19
	v_add_u32_e32 v19, v18, v19
	v_ashrrev_i32_e32 v19, 12, v19
	v_mul_i32_i24_e32 v20, 0x1000, v19
	v_sub_u32_e32 v18, v18, v20
	v_mul_i32_i24_e32 v19, 0x1080, v19
	v_add3_u32 v18, v18, v19, 16
	v_ashrrev_i32_e32 v19, 31, v18
	v_lshlrev_b64 v[18:19], 11, v[18:19]
	v_lshl_add_u64 v[18:19], s[36:37], 0, v[18:19]
	v_lshl_add_u64 v[18:19], v[18:19], 0, v[130:131]
	v_cvt_pk_bf16_f32 v6, v6, v7
	v_cvt_pk_bf16_f32 v7, v8, v9
	v_cvt_pk_bf16_f32 v8, v2, v3
	v_cvt_pk_bf16_f32 v9, v4, v5
	global_store_dwordx4 v[18:19], v[6:9], off sc1
	v_cvt_pk_bf16_f32 v2, v14, v15
	v_cvt_pk_bf16_f32 v3, v16, v17
	v_cvt_pk_bf16_f32 v4, v10, v11
	v_cvt_pk_bf16_f32 v5, v12, v13
	global_store_dwordx4 v[18:19], v[2:5], off offset:256 sc1
	s_cbranch_vccnz .LBB0_503
	s_andn2_b64 vcc, exec, s[10:11]
	s_cbranch_vccnz .LBB0_502
	s_barrier
	s_branch .LBB0_502

; #define LAS __attribute__((address_space(3)))
; __device__ __forceinline__ unsigned cvt_pk_bf16(float lo, float hi) { unsigned r; asm volatile("v_cvt_pk_bf16_f32 %0, %1, %2" : "=v"(r) : "v"(lo), "v"(hi)); return r; }
;     __device__ void operator()(int r, int n, float v) const { if (r < NMETA) proj[(size_t)(M + r) * DINP + n] = f2bf(v); }
;     __device__ __forceinline__ void operator()(const f32x4 (&acc)[2][2][4][2], const Unit& u, int wr, int wc, int fr, int fq, const LAS float* bl) const {
;         const int f0 = u.pm * BM + wr * 64 + fr, tk0 = u.pn * BM + wc * 32 + 8 * fq;
; #pragma unroll
;         for (int ai = 0; ai < 2; ++ai)
; #pragma unroll
;             for (int m = 0; m < 4; ++m) { const int f = f0 + ai * HALF + m * 16;
; #pragma unroll
;                 for (int bj = 0; bj < 2; ++bj) { const int tk = tk0 + bj * HALF, b = tk / S, t = tk % S; const f32x4 v0 = acc[ai][bj][m][0], v1 = acc[ai][bj][m][1];
;                     u32x4 w; w.x = cvt_pk_bf16(v0[0], v0[1]); w.y = cvt_pk_bf16(v0[2], v0[3]); w.z = cvt_pk_bf16(v1[0], v1[1]); w.w = cvt_pk_bf16(v1[2], v1[3]);
;                     *(u32x4*)(vt + ((size_t)b * (NH * 128) + f) * LP + NMETA + t) = w; } }
;     }
.LBB0_560:
	v_lshl_or_b32 v140, s64, 8, v218
	v_ashrrev_i32_e32 v131, 31, v140
	v_lshrrev_b32_e32 v141, 20, v131
	v_add_u32_e32 v131, v140, v141
	v_ashrrev_i32_e32 v136, 12, v131
	v_lshl_add_u32 v130, s83, 8, v217
	v_mul_i32_i24_e32 v131, 0x1000, v136
	v_ashrrev_i32_e32 v137, 31, v136
	v_sub_u32_e32 v138, v140, v131
	v_ashrrev_i32_e32 v131, 31, v130
	v_cvt_pk_bf16_f32 v132, v126, v127
	v_cvt_pk_bf16_f32 v133, v128, v129
	v_cvt_pk_bf16_f32 v134, v122, v123
	v_cvt_pk_bf16_f32 v135, v124, v125
	v_lshlrev_b64 v[124:125], 10, v[136:137]
	v_lshl_add_u64 v[126:127], v[124:125], 0, v[130:131]
	v_mov_b64_e32 v[122:123], s[38:39]
	v_mad_u64_u32 v[128:129], s[6:7], v126, s81, v[122:123]
	v_ashrrev_i32_e32 v139, 31, v138
	v_mad_i32_i24 v129, v127, s81, v129
	v_lshlrev_b64 v[126:127], 1, v[138:139]
	v_lshl_add_u64 v[128:129], v[128:129], 0, v[126:127]
	global_store_dwordx4 v[128:129], v[132:135], off offset:32 sc1
	v_or_b32_e32 v129, 0x80, v140
	v_add_u32_e32 v128, v129, v141
	v_ashrrev_i32_e32 v128, 12, v128
	v_mul_i32_i24_e32 v132, 0x1000, v128
	v_sub_u32_e32 v132, v129, v132
	v_ashrrev_i32_e32 v129, 31, v128
	v_cvt_pk_bf16_f32 v118, v118, v119
	v_cvt_pk_bf16_f32 v119, v120, v121
	v_cvt_pk_bf16_f32 v120, v114, v115
	v_lshlrev_b64 v[114:115], 10, v[128:129]
	v_cvt_pk_bf16_f32 v121, v116, v117
	v_lshl_add_u64 v[116:117], v[114:115], 0, v[130:131]
	v_mad_u64_u32 v[128:129], s[6:7], v116, s81, v[122:123]
	v_ashrrev_i32_e32 v133, 31, v132
	v_mad_i32_i24 v129, v117, s81, v129
	v_lshlrev_b64 v[116:117], 1, v[132:133]
	v_lshl_add_u64 v[128:129], v[128:129], 0, v[116:117]
	global_store_dwordx4 v[128:129], v[118:121], off offset:32 sc1
	v_cvt_pk_bf16_f32 v110, v110, v111
	v_cvt_pk_bf16_f32 v111, v112, v113
	v_cvt_pk_bf16_f32 v112, v106, v107
	v_cvt_pk_bf16_f32 v113, v108, v109
	s_andn2_b64 vcc, exec, s[4:5]
	s_nop 0
	v_or_b32_e32 v118, 16, v130
	v_ashrrev_i32_e32 v119, 31, v118
	v_lshl_add_u64 v[106:107], v[124:125], 0, v[118:119]
	v_mad_u64_u32 v[108:109], s[6:7], v106, s81, v[122:123]
	v_mad_i32_i24 v109, v107, s81, v109
	v_lshl_add_u64 v[106:107], v[108:109], 0, v[126:127]
	global_store_dwordx4 v[106:107], v[110:113], off offset:32 sc1
	v_cvt_pk_bf16_f32 v102, v102, v103
	v_cvt_pk_bf16_f32 v103, v104, v105
	v_cvt_pk_bf16_f32 v104, v98, v99
	v_lshl_add_u64 v[98:99], v[114:115], 0, v[118:119]
	v_cvt_pk_bf16_f32 v105, v100, v101
	v_mad_u64_u32 v[100:101], s[6:7], v98, s81, v[122:123]
	v_mad_i32_i24 v101, v99, s81, v101
	v_lshl_add_u64 v[98:99], v[100:101], 0, v[116:117]
	global_store_dwordx4 v[98:99], v[102:105], off offset:32 sc1
	v_or_b32_e32 v98, 32, v130
	v_ashrrev_i32_e32 v99, 31, v98
	v_cvt_pk_bf16_f32 v94, v94, v95
	v_cvt_pk_bf16_f32 v95, v96, v97
	v_cvt_pk_bf16_f32 v96, v90, v91
	v_lshl_add_u64 v[90:91], v[124:125], 0, v[98:99]
	v_cvt_pk_bf16_f32 v97, v92, v93
	v_mad_u64_u32 v[92:93], s[6:7], v90, s81, v[122:123]
	v_mad_i32_i24 v93, v91, s81, v93
	v_lshl_add_u64 v[90:91], v[92:93], 0, v[126:127]
	global_store_dwordx4 v[90:91], v[94:97], off offset:32 sc1
	v_cvt_pk_bf16_f32 v86, v86, v87
	v_cvt_pk_bf16_f32 v87, v88, v89
	v_cvt_pk_bf16_f32 v88, v82, v83
	v_lshl_add_u64 v[82:83], v[114:115], 0, v[98:99]
	v_cvt_pk_bf16_f32 v89, v84, v85
	v_mad_u64_u32 v[84:85], s[6:7], v82, s81, v[122:123]
	v_mad_i32_i24 v85, v83, s81, v85
	v_lshl_add_u64 v[82:83], v[84:85], 0, v[116:117]
	global_store_dwordx4 v[82:83], v[86:89], off offset:32 sc1
	v_or_b32_e32 v82, 48, v130
	v_ashrrev_i32_e32 v83, 31, v82
	v_cvt_pk_bf16_f32 v78, v78, v79
	v_cvt_pk_bf16_f32 v79, v80, v81
	v_cvt_pk_bf16_f32 v80, v74, v75
	v_lshl_add_u64 v[74:75], v[124:125], 0, v[82:83]
	v_cvt_pk_bf16_f32 v81, v76, v77
	v_mad_u64_u32 v[76:77], s[6:7], v74, s81, v[122:123]
	v_mad_i32_i24 v77, v75, s81, v77
	v_lshl_add_u64 v[74:75], v[76:77], 0, v[126:127]
	global_store_dwordx4 v[74:75], v[78:81], off offset:32 sc1
; #define LAS __attribute__((address_space(3)))
; __device__ __forceinline__ unsigned cvt_pk_bf16(float lo, float hi) { unsigned r; asm volatile("v_cvt_pk_bf16_f32 %0, %1, %2" : "=v"(r) : "v"(lo), "v"(hi)); return r; }
;     __device__ void operator()(int r, int n, float v) const { if (r < NMETA) proj[(size_t)(M + r) * DINP + n] = f2bf(v); }
;     __device__ __forceinline__ void operator()(const f32x4 (&acc)[2][2][4][2], const Unit& u, int wr, int wc, int fr, int fq, const LAS float* bl) const {
;         const int f0 = u.pm * BM + wr * 64 + fr, tk0 = u.pn * BM + wc * 32 + 8 * fq;
; #pragma unroll
;         for (int ai = 0; ai < 2; ++ai)
; #pragma unroll
;             for (int m = 0; m < 4; ++m) { const int f = f0 + ai * HALF + m * 16;
; #pragma unroll
;                 for (int bj = 0; bj < 2; ++bj) { const int tk = tk0 + bj * HALF, b = tk / S, t = tk % S; const f32x4 v0 = acc[ai][bj][m][0], v1 = acc[ai][bj][m][1];
;                     u32x4 w; w.x = cvt_pk_bf16(v0[0], v0[1]); w.y = cvt_pk_bf16(v0[2], v0[3]); w.z = cvt_pk_bf16(v1[0], v1[1]); w.w = cvt_pk_bf16(v1[2], v1[3]);
;                     *(u32x4*)(vt + ((size_t)b * (NH * 128) + f) * LP + NMETA + t) = w; } }
;     }
	v_cvt_pk_bf16_f32 v70, v70, v71
	v_cvt_pk_bf16_f32 v71, v72, v73
	v_cvt_pk_bf16_f32 v72, v66, v67
	v_lshl_add_u64 v[66:67], v[114:115], 0, v[82:83]
	v_cvt_pk_bf16_f32 v73, v68, v69
	v_mad_u64_u32 v[68:69], s[6:7], v66, s81, v[122:123]
	v_mad_i32_i24 v69, v67, s81, v69
	v_lshl_add_u64 v[66:67], v[68:69], 0, v[116:117]
	global_store_dwordx4 v[66:67], v[70:73], off offset:32 sc1
	v_add_u32_e32 v66, 0x80, v130
	v_ashrrev_i32_e32 v67, 31, v66
	v_cvt_pk_bf16_f32 v62, v62, v63
	v_cvt_pk_bf16_f32 v63, v64, v65
	v_cvt_pk_bf16_f32 v64, v58, v59
	v_lshl_add_u64 v[58:59], v[124:125], 0, v[66:67]
	v_cvt_pk_bf16_f32 v65, v60, v61
	v_mad_u64_u32 v[60:61], s[6:7], v58, s81, v[122:123]
	v_mad_i32_i24 v61, v59, s81, v61
	v_lshl_add_u64 v[58:59], v[60:61], 0, v[126:127]
	global_store_dwordx4 v[58:59], v[62:65], off offset:32 sc1
	v_cvt_pk_bf16_f32 v54, v54, v55
	v_cvt_pk_bf16_f32 v55, v56, v57
	v_cvt_pk_bf16_f32 v56, v50, v51
	v_lshl_add_u64 v[50:51], v[114:115], 0, v[66:67]
	v_cvt_pk_bf16_f32 v57, v52, v53
	v_mad_u64_u32 v[52:53], s[6:7], v50, s81, v[122:123]
	v_mad_i32_i24 v53, v51, s81, v53
	v_lshl_add_u64 v[50:51], v[52:53], 0, v[116:117]
	global_store_dwordx4 v[50:51], v[54:57], off offset:32 sc1
	v_add_u32_e32 v50, 0x90, v130
	v_ashrrev_i32_e32 v51, 31, v50
	v_cvt_pk_bf16_f32 v46, v46, v47
	v_cvt_pk_bf16_f32 v47, v48, v49
	v_cvt_pk_bf16_f32 v48, v42, v43
	v_lshl_add_u64 v[42:43], v[124:125], 0, v[50:51]
	v_cvt_pk_bf16_f32 v49, v44, v45
	v_mad_u64_u32 v[44:45], s[6:7], v42, s81, v[122:123]
	v_mad_i32_i24 v45, v43, s81, v45
	v_lshl_add_u64 v[42:43], v[44:45], 0, v[126:127]
	global_store_dwordx4 v[42:43], v[46:49], off offset:32 sc1
	v_cvt_pk_bf16_f32 v38, v38, v39
	v_cvt_pk_bf16_f32 v39, v40, v41
	v_cvt_pk_bf16_f32 v40, v34, v35
	v_lshl_add_u64 v[34:35], v[114:115], 0, v[50:51]
	v_cvt_pk_bf16_f32 v41, v36, v37
	v_mad_u64_u32 v[36:37], s[6:7], v34, s81, v[122:123]
	v_mad_i32_i24 v37, v35, s81, v37
	v_lshl_add_u64 v[34:35], v[36:37], 0, v[116:117]
	global_store_dwordx4 v[34:35], v[38:41], off offset:32 sc1
	v_add_u32_e32 v34, 0xa0, v130
	v_ashrrev_i32_e32 v35, 31, v34
	v_cvt_pk_bf16_f32 v26, v26, v27
	v_cvt_pk_bf16_f32 v27, v28, v29
	v_cvt_pk_bf16_f32 v28, v18, v19
	v_lshl_add_u64 v[18:19], v[124:125], 0, v[34:35]
	v_cvt_pk_bf16_f32 v29, v20, v21
	v_mad_u64_u32 v[20:21], s[6:7], v18, s81, v[122:123]
	v_mad_i32_i24 v21, v19, s81, v21
	v_lshl_add_u64 v[18:19], v[20:21], 0, v[126:127]
	global_store_dwordx4 v[18:19], v[26:29], off offset:32 sc1
	v_cvt_pk_bf16_f32 v18, v30, v31
	v_cvt_pk_bf16_f32 v19, v32, v33
	v_cvt_pk_bf16_f32 v20, v22, v23
	v_lshl_add_u64 v[22:23], v[114:115], 0, v[34:35]
	v_cvt_pk_bf16_f32 v21, v24, v25
	v_mad_u64_u32 v[24:25], s[6:7], v22, s81, v[122:123]
	v_mad_i32_i24 v25, v23, s81, v25
	v_lshl_add_u64 v[22:23], v[24:25], 0, v[116:117]
	global_store_dwordx4 v[22:23], v[18:21], off offset:32 sc1
	v_cvt_pk_bf16_f32 v6, v6, v7
	v_cvt_pk_bf16_f32 v7, v8, v9
	v_cvt_pk_bf16_f32 v8, v2, v3
	v_cvt_pk_bf16_f32 v9, v4, v5
	s_mov_b64 s[4:5], -1
	s_nop 0
	v_add_u32_e32 v18, 0xb0, v130
	v_ashrrev_i32_e32 v19, 31, v18
	v_lshl_add_u64 v[2:3], v[124:125], 0, v[18:19]
	v_mad_u64_u32 v[4:5], s[6:7], v2, s81, v[122:123]
	v_mad_i32_i24 v5, v3, s81, v5
	v_lshl_add_u64 v[2:3], v[4:5], 0, v[126:127]
	global_store_dwordx4 v[2:3], v[6:9], off offset:32 sc1
	v_cvt_pk_bf16_f32 v2, v14, v15
	v_cvt_pk_bf16_f32 v3, v16, v17
	v_cvt_pk_bf16_f32 v4, v10, v11
	v_cvt_pk_bf16_f32 v5, v12, v13
	s_nop 1
	v_lshl_add_u64 v[6:7], v[114:115], 0, v[18:19]
	v_mad_u64_u32 v[8:9], s[6:7], v6, s81, v[122:123]
	v_mad_i32_i24 v9, v7, s81, v9
	v_lshl_add_u64 v[6:7], v[8:9], 0, v[116:117]
	global_store_dwordx4 v[6:7], v[2:5], off offset:32 sc1
	s_cbranch_vccnz .LBB0_539
	s_andn2_b64 vcc, exec, s[10:11]
	s_cbranch_vccnz .LBB0_538
	s_barrier
	s_branch .LBB0_538

; #define LAS __attribute__((address_space(3)))
; __device__ __forceinline__ unsigned cvt_pk_bf16(float lo, float hi) { unsigned r; asm volatile("v_cvt_pk_bf16_f32 %0, %1, %2" : "=v"(r) : "v"(lo), "v"(hi)); return r; }
;     __device__ void operator()(int r, int n, float v) const { if (r < NMETA) proj[(size_t)(M + r) * DINP + n] = f2bf(v); }
;     __device__ __forceinline__ void operator()(const f32x4 (&acc)[2][2][4][2], const Unit& u, int wr, int wc, int fr, int fq, const LAS float* bl) const {
;         const int row0 = u.pm * BM + wr * 64 + fr, col0 = u.pn * BM + wc * 32 + 8 * fq;
;         const LAS float* bias = bl + wc * 32 + 8 * fq;
;         f32x4 bv[2][2];
; #pragma unroll
;         for (int bj = 0; bj < 2; ++bj)
; #pragma unroll
;             for (int n = 0; n < 2; ++n) bv[bj][n] = *(const LAS f32x4*)(bias + bj * HALF + 4 * n);
; #pragma unroll
;         for (int ai = 0; ai < 2; ++ai)
; #pragma unroll
;             for (int m = 0; m < 4; ++m) { bf16* rowp = y + (size_t)(row0 + ai * HALF + m * 16) * D + col0;
; #pragma unroll
;                 for (int bj = 0; bj < 2; ++bj) { f32x4 v0, v1;
; #pragma unroll
;                     for (int h = 0; h < 2; ++h) { const f32x4 a0 = acc[ai][bj][m][0], a1 = acc[ai][bj][m][1], b0 = bv[bj][0], b1 = bv[bj][1];
;                         const f32x2 p0 = __builtin_elementwise_fma((f32x2){a0[2 * h], a0[2 * h + 1]}, (f32x2){WINV, WINV}, (f32x2){b0[2 * h], b0[2 * h + 1]});
;                         const f32x2 p1 = __builtin_elementwise_fma((f32x2){a1[2 * h], a1[2 * h + 1]}, (f32x2){WINV, WINV}, (f32x2){b1[2 * h], b1[2 * h + 1]});
;                         v0[2 * h] = p0.x; v0[2 * h + 1] = p0.y; v1[2 * h] = p1.x; v1[2 * h + 1] = p1.y; }
;                     u32x4 w; w.x = cvt_pk_bf16(v0[0], v0[1]); w.y = cvt_pk_bf16(v0[2], v0[3]); w.z = cvt_pk_bf16(v1[0], v1[1]); w.w = cvt_pk_bf16(v1[2], v1[3]);
;                     *(u32x4*)(rowp + bj * HALF) = w; } }
.LBB0_1518:
	s_lshl_b32 s6, s94, 10
	s_and_b32 s6, s6, 0x400
	v_lshl_add_u32 v24, s93, 8, v211
	v_add_u32_e32 v2, s6, v212
	v_lshl_or_b32 v18, s54, 8, v213
	v_ashrrev_i32_e32 v25, 31, v24
	ds_read_b128 v[14:17], v2
	ds_read_b128 v[10:13], v2 offset:16
	ds_read_b128 v[6:9], v2 offset:512
	ds_read_b128 v[2:5], v2 offset:528
	v_ashrrev_i32_e32 v19, 31, v18
	v_lshlrev_b64 v[20:21], 12, v[24:25]
	v_lshl_add_u64 v[20:21], s[26:27], 0, v[20:21]
	v_lshlrev_b64 v[26:27], 1, v[18:19]
	v_lshl_add_u64 v[18:19], v[20:21], 0, v[26:27]
	s_waitcnt lgkmcnt(0)
	v_pk_fma_f32 v[20:21], v[190:191], s[36:37], v[14:15] op_sel_hi:[1,0,1]
	v_pk_fma_f32 v[22:23], v[186:187], s[36:37], v[10:11] op_sel_hi:[1,0,1]
	v_pk_fma_f32 v[28:29], v[192:193], s[36:37], v[16:17] op_sel_hi:[1,0,1]
	v_cvt_pk_bf16_f32 v20, v20, v21
	v_pk_fma_f32 v[30:31], v[188:189], s[36:37], v[12:13] op_sel_hi:[1,0,1]
	v_cvt_pk_bf16_f32 v21, v28, v29
	v_cvt_pk_bf16_f32 v22, v22, v23
	v_pk_fma_f32 v[28:29], v[184:185], s[36:37], v[8:9] op_sel_hi:[1,0,1]
	v_cvt_pk_bf16_f32 v23, v30, v31
	global_store_dwordx4 v[18:19], v[20:23], off sc1
	v_pk_fma_f32 v[30:31], v[180:181], s[36:37], v[4:5] op_sel_hi:[1,0,1]
	v_pk_fma_f32 v[32:33], v[172:173], s[36:37], v[12:13] op_sel_hi:[1,0,1]
	v_pk_fma_f32 v[20:21], v[182:183], s[36:37], v[6:7] op_sel_hi:[1,0,1]
	v_pk_fma_f32 v[22:23], v[178:179], s[36:37], v[2:3] op_sel_hi:[1,0,1]
	v_cvt_pk_bf16_f32 v20, v20, v21
	v_cvt_pk_bf16_f32 v21, v28, v29
	s_mov_b64 s[6:7], -1
	v_cvt_pk_bf16_f32 v22, v22, v23
	v_cvt_pk_bf16_f32 v23, v30, v31
	global_store_dwordx4 v[18:19], v[20:23], off offset:256 sc1
	v_pk_fma_f32 v[30:31], v[176:177], s[36:37], v[16:17] op_sel_hi:[1,0,1]
	s_nop 0
	v_or_b32_e32 v20, 16, v24
	v_ashrrev_i32_e32 v21, 31, v20
	v_lshlrev_b64 v[20:21], 12, v[20:21]
	v_lshl_add_u64 v[20:21], s[26:27], 0, v[20:21]
	v_lshl_add_u64 v[28:29], v[20:21], 0, v[26:27]
	v_pk_fma_f32 v[20:21], v[174:175], s[36:37], v[14:15] op_sel_hi:[1,0,1]
	v_pk_fma_f32 v[22:23], v[170:171], s[36:37], v[10:11] op_sel_hi:[1,0,1]
	v_cvt_pk_bf16_f32 v20, v20, v21
	v_cvt_pk_bf16_f32 v21, v30, v31
	v_pk_fma_f32 v[30:31], v[168:169], s[36:37], v[8:9] op_sel_hi:[1,0,1]
	v_cvt_pk_bf16_f32 v22, v22, v23
	v_cvt_pk_bf16_f32 v23, v32, v33
	global_store_dwordx4 v[28:29], v[20:23], off sc1
	v_pk_fma_f32 v[32:33], v[164:165], s[36:37], v[4:5] op_sel_hi:[1,0,1]
	s_nop 0
	v_pk_fma_f32 v[20:21], v[166:167], s[36:37], v[6:7] op_sel_hi:[1,0,1]
	v_pk_fma_f32 v[22:23], v[162:163], s[36:37], v[2:3] op_sel_hi:[1,0,1]
	v_cvt_pk_bf16_f32 v20, v20, v21
	v_cvt_pk_bf16_f32 v21, v30, v31
	v_pk_fma_f32 v[30:31], v[160:161], s[36:37], v[16:17] op_sel_hi:[1,0,1]
	v_cvt_pk_bf16_f32 v22, v22, v23
	v_cvt_pk_bf16_f32 v23, v32, v33
	global_store_dwordx4 v[28:29], v[20:23], off offset:256 sc1
	v_pk_fma_f32 v[32:33], v[156:157], s[36:37], v[12:13] op_sel_hi:[1,0,1]
	s_nop 0
	v_or_b32_e32 v20, 32, v24
	v_ashrrev_i32_e32 v21, 31, v20
	v_lshlrev_b64 v[20:21], 12, v[20:21]
	v_lshl_add_u64 v[20:21], s[26:27], 0, v[20:21]
	v_lshl_add_u64 v[28:29], v[20:21], 0, v[26:27]
	v_pk_fma_f32 v[20:21], v[158:159], s[36:37], v[14:15] op_sel_hi:[1,0,1]
	v_pk_fma_f32 v[22:23], v[154:155], s[36:37], v[10:11] op_sel_hi:[1,0,1]
	v_cvt_pk_bf16_f32 v20, v20, v21
	v_cvt_pk_bf16_f32 v21, v30, v31
	v_pk_fma_f32 v[30:31], v[152:153], s[36:37], v[8:9] op_sel_hi:[1,0,1]
	v_cvt_pk_bf16_f32 v22, v22, v23
	v_cvt_pk_bf16_f32 v23, v32, v33
	global_store_dwordx4 v[28:29], v[20:23], off sc1
	v_pk_fma_f32 v[32:33], v[148:149], s[36:37], v[4:5] op_sel_hi:[1,0,1]
	s_nop 0
	v_pk_fma_f32 v[20:21], v[150:151], s[36:37], v[6:7] op_sel_hi:[1,0,1]
	v_pk_fma_f32 v[22:23], v[146:147], s[36:37], v[2:3] op_sel_hi:[1,0,1]
	v_cvt_pk_bf16_f32 v20, v20, v21
	v_cvt_pk_bf16_f32 v21, v30, v31
	s_nop 0
	v_cvt_pk_bf16_f32 v22, v22, v23
	v_cvt_pk_bf16_f32 v23, v32, v33
	global_store_dwordx4 v[28:29], v[20:23], off offset:256 sc1
	v_pk_fma_f32 v[28:29], v[140:141], s[36:37], v[12:13] op_sel_hi:[1,0,1]
	s_nop 0
	v_or_b32_e32 v20, 48, v24
	v_ashrrev_i32_e32 v21, 31, v20
	v_lshlrev_b64 v[20:21], 12, v[20:21]
	v_lshl_add_u64 v[20:21], s[26:27], 0, v[20:21]
	v_lshl_add_u64 v[24:25], v[20:21], 0, v[26:27]
	v_pk_fma_f32 v[20:21], v[142:143], s[36:37], v[14:15] op_sel_hi:[1,0,1]
	v_pk_fma_f32 v[22:23], v[138:139], s[36:37], v[10:11] op_sel_hi:[1,0,1]
	v_pk_fma_f32 v[26:27], v[144:145], s[36:37], v[16:17] op_sel_hi:[1,0,1]
	v_cvt_pk_bf16_f32 v20, v20, v21
	s_nop 0
	v_cvt_pk_bf16_f32 v21, v26, v27
	v_cvt_pk_bf16_f32 v22, v22, v23
	v_cvt_pk_bf16_f32 v23, v28, v29
	global_store_dwordx4 v[24:25], v[20:23], off sc1
	v_pk_fma_f32 v[26:27], v[136:137], s[36:37], v[8:9] op_sel_hi:[1,0,1]
	v_pk_fma_f32 v[28:29], v[132:133], s[36:37], v[4:5] op_sel_hi:[1,0,1]
	v_pk_fma_f32 v[20:21], v[134:135], s[36:37], v[6:7] op_sel_hi:[1,0,1]
; __device__ __forceinline__ unsigned cvt_pk_bf16(float lo, float hi) { unsigned r; asm volatile("v_cvt_pk_bf16_f32 %0, %1, %2" : "=v"(r) : "v"(lo), "v"(hi)); return r; }
;     __device__ __forceinline__ void operator()(const f32x4 (&acc)[2][2][4][2], const Unit& u, int wr, int wc, int fr, int fq, const LAS float* bl) const {
;     ...
;             for (int m = 0; m < 4; ++m) { bf16* rowp = y + (size_t)(row0 + ai * HALF + m * 16) * D + col0;
; #pragma unroll
;                 for (int bj = 0; bj < 2; ++bj) { f32x4 v0, v1;
; #pragma unroll
;                     for (int h = 0; h < 2; ++h) { const f32x4 a0 = acc[ai][bj][m][0], a1 = acc[ai][bj][m][1], b0 = bv[bj][0], b1 = bv[bj][1];
;                         const f32x2 p0 = __builtin_elementwise_fma((f32x2){a0[2 * h], a0[2 * h + 1]}, (f32x2){WINV, WINV}, (f32x2){b0[2 * h], b0[2 * h + 1]});
;                         const f32x2 p1 = __builtin_elementwise_fma((f32x2){a1[2 * h], a1[2 * h + 1]}, (f32x2){WINV, WINV}, (f32x2){b1[2 * h], b1[2 * h + 1]});
;                         v0[2 * h] = p0.x; v0[2 * h + 1] = p0.y; v1[2 * h] = p1.x; v1[2 * h + 1] = p1.y; }
;                     u32x4 w; w.x = cvt_pk_bf16(v0[0], v0[1]); w.y = cvt_pk_bf16(v0[2], v0[3]); w.z = cvt_pk_bf16(v1[0], v1[1]); w.w = cvt_pk_bf16(v1[2], v1[3]);
;                     *(u32x4*)(rowp + bj * HALF) = w; } }
	v_pk_fma_f32 v[22:23], v[130:131], s[36:37], v[2:3] op_sel_hi:[1,0,1]
	v_cvt_pk_bf16_f32 v20, v20, v21
	v_cvt_pk_bf16_f32 v21, v26, v27
	v_pk_fma_f32 v[26:27], v[128:129], s[36:37], v[16:17] op_sel_hi:[1,0,1]
	v_cvt_pk_bf16_f32 v22, v22, v23
	v_cvt_pk_bf16_f32 v23, v28, v29
	global_store_dwordx4 v[24:25], v[20:23], off offset:256 sc1
	v_pk_fma_f32 v[28:29], v[124:125], s[36:37], v[12:13] op_sel_hi:[1,0,1]
	v_lshl_add_u64 v[24:25], v[18:19], 0, s[38:39]
	v_pk_fma_f32 v[20:21], v[126:127], s[36:37], v[14:15] op_sel_hi:[1,0,1]
	v_pk_fma_f32 v[22:23], v[122:123], s[36:37], v[10:11] op_sel_hi:[1,0,1]
	v_cvt_pk_bf16_f32 v20, v20, v21
	v_cvt_pk_bf16_f32 v21, v26, v27
	v_add_co_u32_e32 v26, vcc, s86, v18
	v_cvt_pk_bf16_f32 v22, v22, v23
	v_cvt_pk_bf16_f32 v23, v28, v29
	v_pk_fma_f32 v[28:29], v[116:117], s[36:37], v[4:5] op_sel_hi:[1,0,1]
	s_nop 0
	v_addc_co_u32_e32 v27, vcc, 0, v19, vcc
	global_store_dwordx4 v[26:27], v[20:23], off sc1
	v_pk_fma_f32 v[26:27], v[120:121], s[36:37], v[8:9] op_sel_hi:[1,0,1]
	s_nop 0
	v_pk_fma_f32 v[20:21], v[118:119], s[36:37], v[6:7] op_sel_hi:[1,0,1]
	v_pk_fma_f32 v[22:23], v[114:115], s[36:37], v[2:3] op_sel_hi:[1,0,1]
	v_cvt_pk_bf16_f32 v20, v20, v21
	v_cvt_pk_bf16_f32 v21, v26, v27
	v_pk_fma_f32 v[26:27], v[112:113], s[36:37], v[16:17] op_sel_hi:[1,0,1]
	v_cvt_pk_bf16_f32 v22, v22, v23
	v_cvt_pk_bf16_f32 v23, v28, v29
	global_store_dwordx4 v[24:25], v[20:23], off offset:256 sc1
	v_pk_fma_f32 v[28:29], v[108:109], s[36:37], v[12:13] op_sel_hi:[1,0,1]
	v_lshl_add_u64 v[24:25], v[18:19], 0, s[40:41]
	v_pk_fma_f32 v[20:21], v[110:111], s[36:37], v[14:15] op_sel_hi:[1,0,1]
	v_pk_fma_f32 v[22:23], v[106:107], s[36:37], v[10:11] op_sel_hi:[1,0,1]
	v_cvt_pk_bf16_f32 v20, v20, v21
	v_cvt_pk_bf16_f32 v21, v26, v27
	v_add_co_u32_e32 v26, vcc, s87, v18
	v_cvt_pk_bf16_f32 v22, v22, v23
	v_cvt_pk_bf16_f32 v23, v28, v29
	v_pk_fma_f32 v[28:29], v[100:101], s[36:37], v[4:5] op_sel_hi:[1,0,1]
	s_nop 0
	v_addc_co_u32_e32 v27, vcc, 0, v19, vcc
	global_store_dwordx4 v[26:27], v[20:23], off sc1
	v_pk_fma_f32 v[26:27], v[104:105], s[36:37], v[8:9] op_sel_hi:[1,0,1]
	s_nop 0
	v_pk_fma_f32 v[20:21], v[102:103], s[36:37], v[6:7] op_sel_hi:[1,0,1]
	v_pk_fma_f32 v[22:23], v[98:99], s[36:37], v[2:3] op_sel_hi:[1,0,1]
	v_cvt_pk_bf16_f32 v20, v20, v21
	v_cvt_pk_bf16_f32 v21, v26, v27
	v_pk_fma_f32 v[26:27], v[96:97], s[36:37], v[16:17] op_sel_hi:[1,0,1]
	v_cvt_pk_bf16_f32 v22, v22, v23
	v_cvt_pk_bf16_f32 v23, v28, v29
	global_store_dwordx4 v[24:25], v[20:23], off offset:256 sc1
	v_pk_fma_f32 v[28:29], v[88:89], s[36:37], v[12:13] op_sel_hi:[1,0,1]
	v_lshl_add_u64 v[24:25], v[18:19], 0, s[42:43]
	v_pk_fma_f32 v[20:21], v[94:95], s[36:37], v[14:15] op_sel_hi:[1,0,1]
	v_pk_fma_f32 v[22:23], v[86:87], s[36:37], v[10:11] op_sel_hi:[1,0,1]
	v_cvt_pk_bf16_f32 v20, v20, v21
	v_cvt_pk_bf16_f32 v21, v26, v27
	v_add_co_u32_e32 v26, vcc, s88, v18
	v_cvt_pk_bf16_f32 v22, v22, v23
	v_cvt_pk_bf16_f32 v23, v28, v29
	v_pk_fma_f32 v[28:29], v[84:85], s[36:37], v[4:5] op_sel_hi:[1,0,1]
	s_nop 0
	v_addc_co_u32_e32 v27, vcc, 0, v19, vcc
	global_store_dwordx4 v[26:27], v[20:23], off sc1
	v_pk_fma_f32 v[26:27], v[92:93], s[36:37], v[8:9] op_sel_hi:[1,0,1]
	v_pk_fma_f32 v[14:15], v[74:75], s[36:37], v[14:15] op_sel_hi:[1,0,1]
	v_pk_fma_f32 v[20:21], v[90:91], s[36:37], v[6:7] op_sel_hi:[1,0,1]
	v_pk_fma_f32 v[22:23], v[82:83], s[36:37], v[2:3] op_sel_hi:[1,0,1]
	v_cvt_pk_bf16_f32 v20, v20, v21
	v_cvt_pk_bf16_f32 v21, v26, v27
	v_pk_fma_f32 v[16:17], v[76:77], s[36:37], v[16:17] op_sel_hi:[1,0,1]
	v_cvt_pk_bf16_f32 v22, v22, v23
	v_cvt_pk_bf16_f32 v23, v28, v29
	global_store_dwordx4 v[24:25], v[20:23], off offset:256 sc1
	v_pk_fma_f32 v[24:25], v[68:69], s[36:37], v[12:13] op_sel_hi:[1,0,1]
	v_pk_fma_f32 v[6:7], v[78:79], s[36:37], v[6:7] op_sel_hi:[1,0,1]
	v_pk_fma_f32 v[22:23], v[66:67], s[36:37], v[10:11] op_sel_hi:[1,0,1]
	v_cvt_pk_bf16_f32 v10, v14, v15
	v_add_co_u32_e32 v14, vcc, s89, v18
	v_lshl_add_u64 v[20:21], v[18:19], 0, s[44:45]
	s_nop 0
	v_addc_co_u32_e32 v15, vcc, 0, v19, vcc
	v_cvt_pk_bf16_f32 v11, v16, v17
	v_cvt_pk_bf16_f32 v12, v22, v23
	v_cvt_pk_bf16_f32 v13, v24, v25
	s_andn2_b64 vcc, exec, s[50:51]
	global_store_dwordx4 v[14:15], v[10:13], off sc1
	v_pk_fma_f32 v[8:9], v[80:81], s[36:37], v[8:9] op_sel_hi:[1,0,1]
	s_nop 0
	v_pk_fma_f32 v[10:11], v[70:71], s[36:37], v[2:3] op_sel_hi:[1,0,1]
	v_pk_fma_f32 v[12:13], v[72:73], s[36:37], v[4:5] op_sel_hi:[1,0,1]
	v_cvt_pk_bf16_f32 v2, v6, v7
	v_cvt_pk_bf16_f32 v3, v8, v9
	v_cvt_pk_bf16_f32 v4, v10, v11
	s_nop 0
	v_cvt_pk_bf16_f32 v5, v12, v13
	global_store_dwordx4 v[20:21], v[2:5], off offset:256 sc1
	s_cbranch_vccnz .LBB0_1492
	s_andn2_b64 vcc, exec, s[16:17]
	s_cbranch_vccnz .LBB0_1491
	s_barrier
	s_branch .LBB0_1491
